# all latency-chain edits stacked: barrier polling, router LDS read pipelining, attention permlane exchanges, split-K tail gate-weight hoist, router prologue unroll and bias hoist
# baseline (speedup 1.0000x reference)
.LBB0_1376:
	v_mov_b32_e32 v78, v43
	v_mov_b32_e32 v79, v45
	v_mov_b32_e32 v76, v42
	v_mov_b32_e32 v77, v44
	v_pk_mul_f32 v[78:79], v[78:79], v[78:79]
	v_mov_b32_e32 v80, v47
	v_mov_b32_e32 v81, v51
	v_pk_fma_f32 v[76:77], v[76:77], v[76:77], v[78:79]
	v_mov_b32_e32 v78, v46
	v_mov_b32_e32 v79, v50
	v_pk_mul_f32 v[80:81], v[80:81], v[80:81]
	v_lshl_add_u64 v[74:75], s[56:57], 0, v[38:39]
	v_pk_fma_f32 v[78:79], v[78:79], v[78:79], v[80:81]
	v_pk_mul_f32 v[80:81], v[48:49], v[48:49]
	v_pk_add_f32 v[76:77], v[76:77], v[78:79]
	v_pk_mul_f32 v[78:79], v[54:55], v[54:55]
	v_pk_add_f32 v[76:77], v[76:77], v[76:77] op_sel:[0,1] op_sel_hi:[1,0]
	v_pk_mov_b32 v[82:83], v[80:81], v[78:79] op_sel:[1,0]
	v_mov_b32_e32 v81, v79
	v_pk_add_f32 v[78:79], v[82:83], v[80:81]
	v_mul_f32_e32 v80, v56, v56
	v_mul_f32_e32 v81, v57, v57
	v_pk_add_f32 v[78:79], v[78:79], v[78:79] op_sel:[0,1] op_sel_hi:[1,0]
	v_mov_b32_e32 v77, v80
	v_mov_b32_e32 v79, v81
	v_pk_add_f32 v[76:77], v[76:77], v[78:79]
	v_mul_f32_e32 v78, v53, v53
	v_mul_f32_e32 v80, v59, v59
	v_mul_f32_e32 v82, v62, v62
	v_mul_f32_e32 v83, v63, v63
	v_pk_fma_f32 v[78:79], v[52:53], v[52:53], v[78:79] op_sel_hi:[1,1,0]
	v_pk_fma_f32 v[80:81], v[58:59], v[58:59], v[80:81] op_sel_hi:[1,1,0]
	v_mov_b32_e32 v79, v82
	v_mov_b32_e32 v81, v83
	v_pk_add_f32 v[78:79], v[78:79], v[80:81]
	v_pk_mul_f32 v[80:81], v[60:61], v[60:61]
	v_pk_add_f32 v[76:77], v[76:77], v[78:79]
	v_pk_mul_f32 v[78:79], v[66:67], v[66:67]
	v_pk_add_f32 v[76:77], v[76:77], v[76:77] op_sel:[0,1] op_sel_hi:[1,0]
	v_pk_mov_b32 v[82:83], v[80:81], v[78:79] op_sel:[1,0]
	v_mov_b32_e32 v81, v79
	v_pk_add_f32 v[78:79], v[82:83], v[80:81]
	v_mul_f32_e32 v80, v68, v68
	v_mul_f32_e32 v81, v69, v69
	v_pk_add_f32 v[78:79], v[78:79], v[78:79] op_sel:[0,1] op_sel_hi:[1,0]
	v_mov_b32_e32 v77, v80
	v_mov_b32_e32 v79, v81
	v_pk_add_f32 v[76:77], v[76:77], v[78:79]
	v_mul_f32_e32 v78, v65, v65
	v_mul_f32_e32 v80, v71, v71
	v_mul_f32_e32 v82, v72, v72
	v_mul_f32_e32 v83, v73, v73
	v_pk_fma_f32 v[78:79], v[64:65], v[64:65], v[78:79] op_sel_hi:[1,1,0]
	v_pk_fma_f32 v[80:81], v[70:71], v[70:71], v[80:81] op_sel_hi:[1,1,0]
	v_mov_b32_e32 v79, v82
	v_mov_b32_e32 v81, v83
	v_pk_add_f32 v[78:79], v[78:79], v[80:81]
	v_add_co_u32_e32 v74, vcc, s11, v74
	v_pk_add_f32 v[76:77], v[76:77], v[78:79]
	s_nop 0
	v_addc_co_u32_e32 v75, vcc, 0, v75, vcc
	v_add_f32_e32 v76, v76, v77
	global_load_dwordx2 v[90:91], v[74:75], off
	global_load_dwordx2 v[88:89], v[74:75], off offset:512
	global_load_dwordx2 v[82:83], v[74:75], off offset:1024
	global_load_dwordx2 v[80:81], v[74:75], off offset:1536
	v_add_f32_dpp v76, v76, v76 quad_perm:[1,0,3,2] row_mask:0xf bank_mask:0xf bound_ctrl:1
	v_mov_b32_e32 v96, 0
	v_mov_b32_e32 v97, 0
	v_add_f32_dpp v76, v76, v76 quad_perm:[2,3,0,1] row_mask:0xf bank_mask:0xf bound_ctrl:1
	v_mov_b32_e32 v98, 0
	s_nop 0
	v_add_f32_dpp v76, v76, v76 row_half_mirror row_mask:0xf bank_mask:0xf bound_ctrl:1
	s_nop 1
	v_add_f32_dpp v76, v76, v76 row_mirror row_mask:0xf bank_mask:0xf bound_ctrl:1
	s_nop 0
	v_readlane_b32 s6, v76, 16
	v_readlane_b32 s7, v76, 48
	v_readlane_b32 s0, v76, 0
	v_readlane_b32 s1, v76, 32
	v_mov_b32_e32 v76, s6
	v_mov_b32_e32 v77, s7
	v_pk_add_f32 v[76:77], s[0:1], v[76:77]
	s_nop 0
	v_add_f32_e32 v76, v76, v77
	v_fmamk_f32 v76, v76, 0x3a000000, v111
	v_mul_f32_e32 v77, 0x4f800000, v76
	v_cmp_gt_f32_e32 vcc, s35, v76
	s_nop 1
	v_cndmask_b32_e32 v76, v76, v77, vcc
	v_sqrt_f32_e32 v77, v76
	s_nop 0
	v_add_u32_e32 v78, -1, v77
	v_fma_f32 v79, -v78, v77, v76
	v_cmp_ge_f32_e64 s[0:1], 0, v79
	v_add_u32_e32 v79, 1, v77
	s_nop 0
	v_cndmask_b32_e64 v78, v77, v78, s[0:1]
	v_fma_f32 v77, -v79, v77, v76
	v_cmp_lt_f32_e64 s[0:1], 0, v77
	s_nop 1
	v_cndmask_b32_e64 v77, v78, v79, s[0:1]
	v_mul_f32_e32 v78, 0x37800000, v77
	v_cndmask_b32_e32 v77, v77, v78, vcc
	v_cmp_class_f32_e32 vcc, v76, v112
	s_nop 1
	v_cndmask_b32_e32 v92, v77, v76, vcc
	v_div_scale_f32 v93, s[0:1], v92, v92, 1.0
	v_rcp_f32_e32 v94, v93
	global_load_dwordx2 v[86:87], v[74:75], off offset:2048
	global_load_dwordx2 v[84:85], v[74:75], off offset:2560
	global_load_dwordx2 v[78:79], v[74:75], off offset:3072
	global_load_dwordx2 v[76:77], v[74:75], off offset:3584
	v_fma_f32 v74, -v93, v94, 1.0
	v_fmac_f32_e32 v94, v74, v94
	v_div_scale_f32 v74, vcc, 1.0, v92, 1.0
	v_mul_f32_e32 v75, v74, v94
	v_fma_f32 v95, -v93, v75, v74
	v_fmac_f32_e32 v75, v95, v94
	v_fma_f32 v74, -v93, v75, v74
	v_div_fmas_f32 v74, v74, v94, v75
	v_div_fixup_f32 v92, v74, v92, 1.0
	v_pk_mul_f32 v[42:43], v[92:93], v[42:43] op_sel_hi:[0,1]
	s_waitcnt vmcnt(12)
	v_pk_mul_f32 v[42:43], v[42:43], v[14:15]
	v_pk_mul_f32 v[46:47], v[92:93], v[46:47] op_sel_hi:[0,1]
	v_med3_f32 v93, v42, s60, v115
	v_med3_f32 v94, v43, s60, v115
	v_mov_b32_e32 v95, 0
	v_cvt_pk_fp8_f32 v95, v93, v94
	v_pk_mul_f32 v[46:47], v[46:47], v[16:17]
	v_lshl_add_u64 v[74:75], s[56:57], 0, v[40:41]
	v_med3_f32 v93, v46, s60, v115
	v_med3_f32 v94, v47, s60, v115
	v_cvt_pk_fp8_f32 v95, v93, v94 op_sel:[0,0,1]
	v_add_co_u32_e32 v74, vcc, s61, v74
	v_pk_mul_f32 v[44:45], v[92:93], v[44:45] op_sel_hi:[0,1]
	s_nop 0
	v_addc_co_u32_e32 v75, vcc, 0, v75, vcc
	v_pk_mul_f32 v[44:45], v[44:45], v[2:3]
	global_store_dword v[74:75], v95, off
	v_pk_mul_f32 v[50:51], v[92:93], v[50:51] op_sel_hi:[0,1]
	v_med3_f32 v93, v44, s60, v115
	v_med3_f32 v94, v45, s60, v115
	v_mov_b32_e32 v95, 0
	v_cvt_pk_fp8_f32 v95, v93, v94
	v_pk_mul_f32 v[50:51], v[50:51], v[4:5]
	s_nop 0
	v_med3_f32 v93, v50, s60, v115
	v_pk_mul_f32 v[48:49], v[92:93], v[48:49] op_sel_hi:[0,1]
	v_med3_f32 v94, v51, s60, v115
	v_pk_mul_f32 v[48:49], v[48:49], v[6:7]
	v_cvt_pk_fp8_f32 v95, v93, v94 op_sel:[0,0,1]
	v_pk_mul_f32 v[54:55], v[92:93], v[54:55] op_sel_hi:[0,1]
	v_med3_f32 v93, v48, s60, v115
	v_med3_f32 v94, v49, s60, v115
	v_cvt_pk_fp8_f32 v96, v93, v94
	v_pk_mul_f32 v[54:55], v[54:55], v[8:9]
	s_nop 0
	v_med3_f32 v93, v54, s60, v115
	v_pk_mul_f32 v[52:53], v[92:93], v[52:53] op_sel_hi:[0,1]
	v_med3_f32 v94, v55, s60, v115
	v_pk_mul_f32 v[52:53], v[52:53], v[10:11]
	v_cvt_pk_fp8_f32 v96, v93, v94 op_sel:[0,0,1]
	v_pk_mul_f32 v[58:59], v[92:93], v[58:59] op_sel_hi:[0,1]
	v_med3_f32 v93, v52, s60, v115
	v_med3_f32 v94, v53, s60, v115
	v_cvt_pk_fp8_f32 v97, v93, v94
	v_pk_mul_f32 v[58:59], v[58:59], v[12:13]
	s_nop 0
	v_med3_f32 v93, v58, s60, v115
	v_pk_mul_f32 v[56:57], v[92:93], v[56:57] op_sel_hi:[0,1]
	v_med3_f32 v94, v59, s60, v115
	s_waitcnt vmcnt(12)
	v_pk_mul_f32 v[56:57], v[56:57], v[18:19]
	v_cvt_pk_fp8_f32 v97, v93, v94 op_sel:[0,0,1]
	v_pk_mul_f32 v[62:63], v[92:93], v[62:63] op_sel_hi:[0,1]
	v_med3_f32 v93, v56, s60, v115
	v_med3_f32 v94, v57, s60, v115
	v_cvt_pk_fp8_f32 v98, v93, v94
	v_pk_mul_f32 v[62:63], v[62:63], v[20:21]
	s_nop 0
	v_med3_f32 v93, v62, s60, v115
	v_med3_f32 v94, v63, s60, v115
	v_pk_mul_f32 v[60:61], v[92:93], v[60:61] op_sel_hi:[0,1]
	v_cvt_pk_fp8_f32 v98, v93, v94 op_sel:[0,0,1]
	s_waitcnt vmcnt(11)
	v_pk_mul_f32 v[60:61], v[60:61], v[22:23]
	global_store_dword v[74:75], v95, off offset:256
	global_store_dword v[74:75], v96, off offset:512
	global_store_dword v[74:75], v97, off offset:768
	global_store_dword v[74:75], v98, off offset:1024
	v_pk_mul_f32 v[66:67], v[92:93], v[66:67] op_sel_hi:[0,1]
	v_med3_f32 v93, v60, s60, v115
	v_med3_f32 v94, v61, s60, v115
	v_mov_b32_e32 v96, 0
	v_cvt_pk_fp8_f32 v96, v93, v94
	v_pk_mul_f32 v[66:67], v[66:67], v[24:25]
	v_mov_b32_e32 v97, 0
	v_med3_f32 v93, v66, s60, v115
	v_pk_mul_f32 v[64:65], v[92:93], v[64:65] op_sel_hi:[0,1]
	v_med3_f32 v94, v67, s60, v115
	s_waitcnt vmcnt(14)
	v_pk_mul_f32 v[64:65], v[64:65], v[26:27]
	v_cvt_pk_fp8_f32 v96, v93, v94 op_sel:[0,0,1]
	v_pk_mul_f32 v[70:71], v[92:93], v[70:71] op_sel_hi:[0,1]
	v_med3_f32 v93, v64, s60, v115
	v_med3_f32 v94, v65, s60, v115
	v_cvt_pk_fp8_f32 v97, v93, v94
	v_pk_mul_f32 v[70:71], v[70:71], v[28:29]
	v_mov_b32_e32 v98, 0
	v_med3_f32 v93, v70, s60, v115
	v_pk_mul_f32 v[68:69], v[92:93], v[68:69] op_sel_hi:[0,1]
	v_med3_f32 v94, v71, s60, v115
	s_waitcnt vmcnt(13)
	v_pk_mul_f32 v[68:69], v[68:69], v[30:31]
	v_cvt_pk_fp8_f32 v97, v93, v94 op_sel:[0,0,1]
	v_pk_mul_f32 v[72:73], v[92:93], v[72:73] op_sel_hi:[0,1]
	v_med3_f32 v92, v68, s60, v115
	v_med3_f32 v93, v69, s60, v115
	v_cvt_pk_fp8_f32 v98, v92, v93
	v_pk_mul_f32 v[72:73], v[72:73], v[32:33]
	s_nop 0
	v_med3_f32 v92, v72, s60, v115
	v_med3_f32 v93, v73, s60, v115
	v_cvt_pk_fp8_f32 v98, v92, v93 op_sel:[0,0,1]
	ds_read_b128 v[150:153], v34 offset:0
	ds_read_b128 v[154:157], v34 offset:1024
	ds_read_b128 v[158:161], v34 offset:2048
	ds_read_b128 v[162:165], v34 offset:3072
	ds_read_b128 v[166:169], v34 offset:4096
	ds_read_b128 v[170:173], v34 offset:5120
	ds_read_b128 v[174:177], v34 offset:6144
	global_store_dword v[74:75], v96, off offset:1280
	global_store_dword v[74:75], v97, off offset:1536
	global_store_dword v[74:75], v98, off offset:1792
	ds_read_b128 v[178:181], v34 offset:7168
	s_waitcnt lgkmcnt(7)
	v_mul_f32_e32 v93, v151, v43
	v_fmac_f32_e32 v93, v150, v42
	v_mul_f32_e32 v92, v153, v47
	v_fmac_f32_e32 v92, v152, v46
	v_add_f32_e32 v92, v93, v92
	v_add_f32_e32 v100, 0, v92
	ds_read_b128 v[150:153], v34 offset:8192
	s_waitcnt lgkmcnt(7)
	v_mul_f32_e32 v97, v155, v45
	v_fmac_f32_e32 v97, v154, v44
	v_mul_f32_e32 v96, v157, v51
	v_fmac_f32_e32 v96, v156, v50
	v_add_f32_e32 v96, v97, v96
	v_add_f32_e32 v100, v100, v96
	ds_read_b128 v[154:157], v34 offset:9216
	s_waitcnt lgkmcnt(7)
	v_mul_f32_e32 v93, v159, v49
	v_fmac_f32_e32 v93, v158, v48
	v_mul_f32_e32 v92, v161, v55
	v_fmac_f32_e32 v92, v160, v54
	v_add_f32_e32 v92, v93, v92
	v_add_f32_e32 v100, v100, v92
	ds_read_b128 v[158:161], v34 offset:10240
	s_waitcnt lgkmcnt(7)
	v_mul_f32_e32 v97, v163, v53
	v_fmac_f32_e32 v97, v162, v52
	v_mul_f32_e32 v96, v165, v59
	v_fmac_f32_e32 v96, v164, v58
	v_add_f32_e32 v96, v97, v96
	v_add_f32_e32 v100, v100, v96
	ds_read_b128 v[162:165], v34 offset:11264
	s_waitcnt lgkmcnt(7)
	v_mul_f32_e32 v93, v167, v57
	v_fmac_f32_e32 v93, v166, v56
	v_mul_f32_e32 v92, v169, v63
	v_fmac_f32_e32 v92, v168, v62
	v_add_f32_e32 v92, v93, v92
	v_add_f32_e32 v100, v100, v92
	ds_read_b128 v[166:169], v34 offset:12288
	s_waitcnt lgkmcnt(7)
	v_mul_f32_e32 v97, v171, v61
	v_fmac_f32_e32 v97, v170, v60
	v_mul_f32_e32 v96, v173, v67
	v_fmac_f32_e32 v96, v172, v66
	v_add_f32_e32 v96, v97, v96
	v_add_f32_e32 v100, v100, v96
	ds_read_b128 v[170:173], v34 offset:13312
	s_waitcnt lgkmcnt(7)
	v_mul_f32_e32 v93, v175, v65
	v_fmac_f32_e32 v93, v174, v64
	v_mul_f32_e32 v92, v177, v71
	v_fmac_f32_e32 v92, v176, v70
	v_add_f32_e32 v92, v93, v92
	s_waitcnt lgkmcnt(6)
	v_mul_f32_e32 v93, v179, v69
	v_mul_f32_e32 v94, v181, v73
	v_fmac_f32_e32 v93, v178, v68
	v_fmac_f32_e32 v94, v180, v72
	v_add_f32_e32 v92, v100, v92
	v_add_f32_e32 v93, v93, v94
	v_add_f32_e32 v92, v92, v93
	s_nop 1
	v_add_f32_dpp v92, v92, v92 quad_perm:[1,0,3,2] row_mask:0xf bank_mask:0xf bound_ctrl:1
	s_nop 1
	v_add_f32_dpp v92, v92, v92 quad_perm:[2,3,0,1] row_mask:0xf bank_mask:0xf bound_ctrl:1
	s_nop 1
	v_add_f32_dpp v92, v92, v92 row_half_mirror row_mask:0xf bank_mask:0xf bound_ctrl:1
	s_nop 1
	v_add_f32_dpp v96, v92, v92 row_mirror row_mask:0xf bank_mask:0xf bound_ctrl:1
	ds_read_b128 v[174:177], v34 offset:14336
	v_readlane_b32 s0, v96, 0
	v_readlane_b32 s39, v96, 16
	v_readlane_b32 s1, v96, 32
	v_readlane_b32 s52, v96, 48
	ds_read_b128 v[178:181], v34 offset:15360
	s_waitcnt lgkmcnt(7)
	v_mul_f32_e32 v93, v151, v43
	v_fmac_f32_e32 v93, v150, v42
	v_mul_f32_e32 v92, v153, v47
	v_fmac_f32_e32 v92, v152, v46
	v_add_f32_e32 v92, v93, v92
	s_waitcnt lgkmcnt(6)
	v_mul_f32_e32 v97, v155, v45
	v_add_f32_e32 v100, 0, v92
	v_fmac_f32_e32 v97, v154, v44
	v_mul_f32_e32 v96, v157, v51
	ds_read_b128 v[150:153], v34 offset:16384
	v_fmac_f32_e32 v96, v156, v50
	v_add_f32_e32 v96, v97, v96
	v_add_f32_e32 v100, v100, v96
	ds_read_b128 v[154:157], v34 offset:17408
	s_waitcnt lgkmcnt(7)
	v_mul_f32_e32 v93, v159, v49
	v_fmac_f32_e32 v93, v158, v48
	v_mul_f32_e32 v92, v161, v55
	v_fmac_f32_e32 v92, v160, v54
	v_add_f32_e32 v92, v93, v92
	s_waitcnt lgkmcnt(6)
	v_mul_f32_e32 v97, v163, v53
	v_add_f32_e32 v100, v100, v92
	v_fmac_f32_e32 v97, v162, v52
	v_mul_f32_e32 v96, v165, v59
	ds_read_b128 v[158:161], v34 offset:18432
	v_fmac_f32_e32 v96, v164, v58
	v_add_f32_e32 v96, v97, v96
	v_add_f32_e32 v100, v100, v96
	ds_read_b128 v[162:165], v34 offset:19456
	s_waitcnt lgkmcnt(7)
	v_mul_f32_e32 v93, v167, v57
	v_fmac_f32_e32 v93, v166, v56
	v_mul_f32_e32 v92, v169, v63
	v_fmac_f32_e32 v92, v168, v62
	v_add_f32_e32 v92, v93, v92
	s_waitcnt lgkmcnt(6)
	v_mul_f32_e32 v97, v171, v61
	v_add_f32_e32 v100, v100, v92
	v_fmac_f32_e32 v97, v170, v60
	v_mul_f32_e32 v96, v173, v67
	ds_read_b128 v[166:169], v34 offset:20480
	v_fmac_f32_e32 v96, v172, v66
	v_add_f32_e32 v96, v97, v96
	v_add_f32_e32 v100, v100, v96
	ds_read_b128 v[170:173], v34 offset:21504
	s_waitcnt lgkmcnt(7)
	v_mul_f32_e32 v93, v175, v65
	v_fmac_f32_e32 v93, v174, v64
	v_mul_f32_e32 v92, v177, v71
	v_fmac_f32_e32 v92, v176, v70
	v_add_f32_e32 v92, v93, v92
	s_waitcnt lgkmcnt(6)
	v_mul_f32_e32 v93, v179, v69
	v_mul_f32_e32 v94, v181, v73
	v_fmac_f32_e32 v93, v178, v68
	v_fmac_f32_e32 v94, v180, v72
	v_add_f32_e32 v92, v100, v92
	v_add_f32_e32 v93, v93, v94
	v_add_f32_e32 v92, v92, v93
	s_nop 1
	v_add_f32_dpp v92, v92, v92 quad_perm:[1,0,3,2] row_mask:0xf bank_mask:0xf bound_ctrl:1
	s_nop 1
	v_add_f32_dpp v92, v92, v92 quad_perm:[2,3,0,1] row_mask:0xf bank_mask:0xf bound_ctrl:1
	s_nop 1
	v_add_f32_dpp v92, v92, v92 row_half_mirror row_mask:0xf bank_mask:0xf bound_ctrl:1
	s_nop 1
	v_add_f32_dpp v96, v92, v92 row_mirror row_mask:0xf bank_mask:0xf bound_ctrl:1
	ds_read_b128 v[174:177], v34 offset:22528
	v_readlane_b32 s6, v96, 0
	v_readlane_b32 s53, v96, 16
	v_readlane_b32 s7, v96, 32
	v_readlane_b32 s63, v96, 48
	ds_read_b128 v[178:181], v34 offset:23552
	s_waitcnt lgkmcnt(7)
	v_mul_f32_e32 v93, v151, v43
	v_fmac_f32_e32 v93, v150, v42
	v_mul_f32_e32 v92, v153, v47
	v_fmac_f32_e32 v92, v152, v46
	v_add_f32_e32 v92, v93, v92
	s_waitcnt lgkmcnt(6)
	v_mul_f32_e32 v97, v155, v45
	v_add_f32_e32 v100, 0, v92
	v_fmac_f32_e32 v97, v154, v44
	v_mul_f32_e32 v96, v157, v51
	ds_read_b128 v[150:153], v34 offset:24576
	v_fmac_f32_e32 v96, v156, v50
	v_add_f32_e32 v96, v97, v96
	v_add_f32_e32 v100, v100, v96
	ds_read_b128 v[154:157], v34 offset:25600
	s_waitcnt lgkmcnt(7)
	v_mul_f32_e32 v93, v159, v49
	v_fmac_f32_e32 v93, v158, v48
	v_mul_f32_e32 v92, v161, v55
	v_fmac_f32_e32 v92, v160, v54
	v_add_f32_e32 v92, v93, v92
	s_waitcnt lgkmcnt(6)
	v_mul_f32_e32 v97, v163, v53
	v_add_f32_e32 v100, v100, v92
	v_fmac_f32_e32 v97, v162, v52
	v_mul_f32_e32 v96, v165, v59
	ds_read_b128 v[158:161], v34 offset:26624
	v_fmac_f32_e32 v96, v164, v58
	v_add_f32_e32 v96, v97, v96
	v_add_f32_e32 v100, v100, v96
	ds_read_b128 v[162:165], v34 offset:27648
	s_waitcnt lgkmcnt(7)
	v_mul_f32_e32 v93, v167, v57
	v_fmac_f32_e32 v93, v166, v56
	v_mul_f32_e32 v92, v169, v63
	v_fmac_f32_e32 v92, v168, v62
	v_add_f32_e32 v92, v93, v92
	s_waitcnt lgkmcnt(6)
	v_mul_f32_e32 v97, v171, v61
	v_add_f32_e32 v100, v100, v92
	v_fmac_f32_e32 v97, v170, v60
	v_mul_f32_e32 v96, v173, v67
	ds_read_b128 v[166:169], v34 offset:28672
	v_fmac_f32_e32 v96, v172, v66
	v_add_f32_e32 v96, v97, v96
	v_add_f32_e32 v100, v100, v96
	ds_read_b128 v[170:173], v34 offset:29696
	s_waitcnt lgkmcnt(7)
	v_mul_f32_e32 v93, v175, v65
	v_fmac_f32_e32 v93, v174, v64
	v_mul_f32_e32 v92, v177, v71
	v_fmac_f32_e32 v92, v176, v70
	v_add_f32_e32 v92, v93, v92
	s_waitcnt lgkmcnt(6)
	v_mul_f32_e32 v93, v179, v69
	v_mul_f32_e32 v94, v181, v73
	v_fmac_f32_e32 v93, v178, v68
	v_fmac_f32_e32 v94, v180, v72
	v_add_f32_e32 v92, v100, v92
	v_add_f32_e32 v93, v93, v94
	v_add_f32_e32 v92, v92, v93
	s_nop 1
	v_add_f32_dpp v92, v92, v92 quad_perm:[1,0,3,2] row_mask:0xf bank_mask:0xf bound_ctrl:1
	s_nop 1
	v_add_f32_dpp v92, v92, v92 quad_perm:[2,3,0,1] row_mask:0xf bank_mask:0xf bound_ctrl:1
	s_nop 1
	v_add_f32_dpp v92, v92, v92 row_half_mirror row_mask:0xf bank_mask:0xf bound_ctrl:1
	s_nop 1
	v_add_f32_dpp v96, v92, v92 row_mirror row_mask:0xf bank_mask:0xf bound_ctrl:1
	ds_read_b128 v[174:177], v34 offset:30720
	v_readlane_b32 s8, v96, 0
	v_readlane_b32 s64, v96, 16
	v_readlane_b32 s9, v96, 32
	v_readlane_b32 s65, v96, 48
	ds_read_b128 v[178:181], v34 offset:31744
	s_waitcnt lgkmcnt(7)
	v_mul_f32_e32 v93, v151, v43
	v_fmac_f32_e32 v93, v150, v42
	v_mul_f32_e32 v92, v153, v47
	v_fmac_f32_e32 v92, v152, v46
	v_add_f32_e32 v92, v93, v92
	s_waitcnt lgkmcnt(6)
	v_mul_f32_e32 v97, v155, v45
	v_add_f32_e32 v100, 0, v92
	v_fmac_f32_e32 v97, v154, v44
	v_mul_f32_e32 v96, v157, v51
	ds_read_b128 v[150:153], v34 offset:32768
	v_fmac_f32_e32 v96, v156, v50
	v_add_f32_e32 v96, v97, v96
	v_add_f32_e32 v100, v100, v96
	ds_read_b128 v[154:157], v34 offset:33792
	s_waitcnt lgkmcnt(7)
	v_mul_f32_e32 v93, v159, v49
	v_fmac_f32_e32 v93, v158, v48
	v_mul_f32_e32 v92, v161, v55
	v_fmac_f32_e32 v92, v160, v54
	v_add_f32_e32 v92, v93, v92
	s_waitcnt lgkmcnt(6)
	v_mul_f32_e32 v97, v163, v53
	v_add_f32_e32 v100, v100, v92
	v_fmac_f32_e32 v97, v162, v52
	v_mul_f32_e32 v96, v165, v59
	ds_read_b128 v[158:161], v34 offset:34816
	v_fmac_f32_e32 v96, v164, v58
	v_add_f32_e32 v96, v97, v96
	v_add_f32_e32 v100, v100, v96
	ds_read_b128 v[162:165], v34 offset:35840
	s_waitcnt lgkmcnt(7)
	v_mul_f32_e32 v93, v167, v57
	v_fmac_f32_e32 v93, v166, v56
	v_mul_f32_e32 v92, v169, v63
	v_fmac_f32_e32 v92, v168, v62
	v_add_f32_e32 v92, v93, v92
	s_waitcnt lgkmcnt(6)
	v_mul_f32_e32 v97, v171, v61
	v_add_f32_e32 v100, v100, v92
	v_fmac_f32_e32 v97, v170, v60
	v_mul_f32_e32 v96, v173, v67
	ds_read_b128 v[166:169], v34 offset:36864
	v_fmac_f32_e32 v96, v172, v66
	v_add_f32_e32 v96, v97, v96
	v_add_f32_e32 v100, v100, v96
	ds_read_b128 v[170:173], v34 offset:37888
	s_waitcnt lgkmcnt(7)
	v_mul_f32_e32 v93, v175, v65
	v_fmac_f32_e32 v93, v174, v64
	v_mul_f32_e32 v92, v177, v71
	v_fmac_f32_e32 v92, v176, v70
	v_add_f32_e32 v92, v93, v92
	s_waitcnt lgkmcnt(6)
	v_mul_f32_e32 v93, v179, v69
	v_mul_f32_e32 v94, v181, v73
	v_fmac_f32_e32 v93, v178, v68
	v_fmac_f32_e32 v94, v180, v72
	v_add_f32_e32 v92, v100, v92
	v_add_f32_e32 v93, v93, v94
	v_add_f32_e32 v92, v92, v93
	s_nop 1
	v_add_f32_dpp v92, v92, v92 quad_perm:[1,0,3,2] row_mask:0xf bank_mask:0xf bound_ctrl:1
	s_nop 1
	v_add_f32_dpp v92, v92, v92 quad_perm:[2,3,0,1] row_mask:0xf bank_mask:0xf bound_ctrl:1
	s_nop 1
	v_add_f32_dpp v92, v92, v92 row_half_mirror row_mask:0xf bank_mask:0xf bound_ctrl:1
	s_nop 1
	v_add_f32_dpp v96, v92, v92 row_mirror row_mask:0xf bank_mask:0xf bound_ctrl:1
	ds_read_b128 v[174:177], v34 offset:38912
	v_readlane_b32 s14, v96, 0
	v_readlane_b32 s66, v96, 16
	v_readlane_b32 s15, v96, 32
	v_readlane_b32 s67, v96, 48
	ds_read_b128 v[178:181], v34 offset:39936
	s_waitcnt lgkmcnt(7)
	v_mul_f32_e32 v93, v151, v43
	v_fmac_f32_e32 v93, v150, v42
	v_mul_f32_e32 v92, v153, v47
	v_fmac_f32_e32 v92, v152, v46
	v_add_f32_e32 v92, v93, v92
	s_waitcnt lgkmcnt(6)
	v_mul_f32_e32 v97, v155, v45
	v_add_f32_e32 v100, 0, v92
	v_fmac_f32_e32 v97, v154, v44
	v_mul_f32_e32 v96, v157, v51
	ds_read_b128 v[150:153], v34 offset:40960
	v_fmac_f32_e32 v96, v156, v50
	v_add_f32_e32 v96, v97, v96
	v_add_f32_e32 v100, v100, v96
	ds_read_b128 v[154:157], v34 offset:41984
	s_waitcnt lgkmcnt(7)
	v_mul_f32_e32 v93, v159, v49
	v_fmac_f32_e32 v93, v158, v48
	v_mul_f32_e32 v92, v161, v55
	v_fmac_f32_e32 v92, v160, v54
	v_add_f32_e32 v92, v93, v92
	s_waitcnt lgkmcnt(6)
	v_mul_f32_e32 v97, v163, v53
	v_add_f32_e32 v100, v100, v92
	v_fmac_f32_e32 v97, v162, v52
	v_mul_f32_e32 v96, v165, v59
	ds_read_b128 v[158:161], v34 offset:43008
	v_fmac_f32_e32 v96, v164, v58
	v_add_f32_e32 v96, v97, v96
	v_add_f32_e32 v100, v100, v96
	ds_read_b128 v[162:165], v34 offset:44032
	s_waitcnt lgkmcnt(7)
	v_mul_f32_e32 v93, v167, v57
	v_fmac_f32_e32 v93, v166, v56
	v_mul_f32_e32 v92, v169, v63
	v_fmac_f32_e32 v92, v168, v62
	v_add_f32_e32 v92, v93, v92
	s_waitcnt lgkmcnt(6)
	v_mul_f32_e32 v97, v171, v61
	v_add_f32_e32 v100, v100, v92
	v_fmac_f32_e32 v97, v170, v60
	v_mul_f32_e32 v96, v173, v67
	ds_read_b128 v[166:169], v34 offset:45056
	v_fmac_f32_e32 v96, v172, v66
	v_add_f32_e32 v96, v97, v96
	v_add_f32_e32 v100, v100, v96
	ds_read_b128 v[170:173], v34 offset:46080
	s_waitcnt lgkmcnt(7)
	v_mul_f32_e32 v93, v175, v65
	v_fmac_f32_e32 v93, v174, v64
	v_mul_f32_e32 v92, v177, v71
	v_fmac_f32_e32 v92, v176, v70
	v_add_f32_e32 v92, v93, v92
	s_waitcnt lgkmcnt(6)
	v_mul_f32_e32 v93, v179, v69
	v_mul_f32_e32 v94, v181, v73
	v_fmac_f32_e32 v93, v178, v68
	v_fmac_f32_e32 v94, v180, v72
	v_add_f32_e32 v92, v100, v92
	v_add_f32_e32 v93, v93, v94
	v_add_f32_e32 v92, v92, v93
	s_nop 1
	v_add_f32_dpp v92, v92, v92 quad_perm:[1,0,3,2] row_mask:0xf bank_mask:0xf bound_ctrl:1
	s_nop 1
	v_add_f32_dpp v92, v92, v92 quad_perm:[2,3,0,1] row_mask:0xf bank_mask:0xf bound_ctrl:1
	s_nop 1
	v_add_f32_dpp v92, v92, v92 row_half_mirror row_mask:0xf bank_mask:0xf bound_ctrl:1
	s_nop 1
	v_add_f32_dpp v96, v92, v92 row_mirror row_mask:0xf bank_mask:0xf bound_ctrl:1
	ds_read_b128 v[174:177], v34 offset:47104
	v_readlane_b32 s16, v96, 0
	v_readlane_b32 s69, v96, 16
	v_readlane_b32 s17, v96, 32
	v_readlane_b32 s70, v96, 48
	ds_read_b128 v[178:181], v34 offset:48128
	s_waitcnt lgkmcnt(7)
	v_mul_f32_e32 v93, v151, v43
	v_fmac_f32_e32 v93, v150, v42
	v_mul_f32_e32 v92, v153, v47
	v_fmac_f32_e32 v92, v152, v46
	v_add_f32_e32 v92, v93, v92
	s_waitcnt lgkmcnt(6)
	v_mul_f32_e32 v97, v155, v45
	v_add_f32_e32 v100, 0, v92
	v_fmac_f32_e32 v97, v154, v44
	v_mul_f32_e32 v96, v157, v51
	ds_read_b128 v[150:153], v34 offset:49152
	v_fmac_f32_e32 v96, v156, v50
	v_add_f32_e32 v96, v97, v96
	v_add_f32_e32 v100, v100, v96
	ds_read_b128 v[154:157], v34 offset:50176
	s_waitcnt lgkmcnt(7)
	v_mul_f32_e32 v93, v159, v49
	v_fmac_f32_e32 v93, v158, v48
	v_mul_f32_e32 v92, v161, v55
	v_fmac_f32_e32 v92, v160, v54
	v_add_f32_e32 v92, v93, v92
	s_waitcnt lgkmcnt(6)
	v_mul_f32_e32 v97, v163, v53
	v_add_f32_e32 v100, v100, v92
	v_fmac_f32_e32 v97, v162, v52
	v_mul_f32_e32 v96, v165, v59
	ds_read_b128 v[158:161], v34 offset:51200
	v_fmac_f32_e32 v96, v164, v58
	v_add_f32_e32 v96, v97, v96
	v_add_f32_e32 v100, v100, v96
	ds_read_b128 v[162:165], v34 offset:52224
	s_waitcnt lgkmcnt(7)
	v_mul_f32_e32 v93, v167, v57
	v_fmac_f32_e32 v93, v166, v56
	v_mul_f32_e32 v92, v169, v63
	v_fmac_f32_e32 v92, v168, v62
	v_add_f32_e32 v92, v93, v92
	s_waitcnt lgkmcnt(6)
	v_mul_f32_e32 v97, v171, v61
	v_add_f32_e32 v100, v100, v92
	v_fmac_f32_e32 v97, v170, v60
	v_mul_f32_e32 v96, v173, v67
	ds_read_b128 v[166:169], v34 offset:53248
	v_fmac_f32_e32 v96, v172, v66
	v_add_f32_e32 v96, v97, v96
	v_add_f32_e32 v100, v100, v96
	ds_read_b128 v[170:173], v34 offset:54272
	s_waitcnt lgkmcnt(7)
	v_mul_f32_e32 v93, v175, v65
	v_fmac_f32_e32 v93, v174, v64
	v_mul_f32_e32 v92, v177, v71
	v_fmac_f32_e32 v92, v176, v70
	v_add_f32_e32 v92, v93, v92
	s_waitcnt lgkmcnt(6)
	v_mul_f32_e32 v93, v179, v69
	v_mul_f32_e32 v94, v181, v73
	v_fmac_f32_e32 v93, v178, v68
	v_fmac_f32_e32 v94, v180, v72
	v_add_f32_e32 v92, v100, v92
	v_add_f32_e32 v93, v93, v94
	v_add_f32_e32 v92, v92, v93
	s_nop 1
	v_add_f32_dpp v92, v92, v92 quad_perm:[1,0,3,2] row_mask:0xf bank_mask:0xf bound_ctrl:1
	s_nop 1
	v_add_f32_dpp v92, v92, v92 quad_perm:[2,3,0,1] row_mask:0xf bank_mask:0xf bound_ctrl:1
	s_nop 1
	v_add_f32_dpp v92, v92, v92 row_half_mirror row_mask:0xf bank_mask:0xf bound_ctrl:1
	s_nop 1
	v_add_f32_dpp v96, v92, v92 row_mirror row_mask:0xf bank_mask:0xf bound_ctrl:1
	ds_read_b128 v[174:177], v34 offset:55296
	v_readlane_b32 s18, v96, 0
	v_readlane_b32 s71, v96, 16
	v_readlane_b32 s19, v96, 32
	v_readlane_b32 s72, v96, 48
	ds_read_b128 v[178:181], v34 offset:56320
	s_waitcnt lgkmcnt(7)
	v_mul_f32_e32 v93, v151, v43
	v_fmac_f32_e32 v93, v150, v42
	v_mul_f32_e32 v92, v153, v47
	v_fmac_f32_e32 v92, v152, v46
	v_add_f32_e32 v92, v93, v92
	s_waitcnt lgkmcnt(6)
	v_mul_f32_e32 v97, v155, v45
	v_add_f32_e32 v100, 0, v92
	v_fmac_f32_e32 v97, v154, v44
	v_mul_f32_e32 v96, v157, v51
	ds_read_b128 v[150:153], v34 offset:57344
	v_fmac_f32_e32 v96, v156, v50
	v_add_f32_e32 v96, v97, v96
	v_add_f32_e32 v100, v100, v96
	ds_read_b128 v[154:157], v34 offset:58368
	s_waitcnt lgkmcnt(7)
	v_mul_f32_e32 v93, v159, v49
	v_fmac_f32_e32 v93, v158, v48
	v_mul_f32_e32 v92, v161, v55
	v_fmac_f32_e32 v92, v160, v54
	v_add_f32_e32 v92, v93, v92
	s_waitcnt lgkmcnt(6)
	v_mul_f32_e32 v97, v163, v53
	v_add_f32_e32 v100, v100, v92
	v_fmac_f32_e32 v97, v162, v52
	v_mul_f32_e32 v96, v165, v59
	ds_read_b128 v[158:161], v34 offset:59392
	v_fmac_f32_e32 v96, v164, v58
	v_add_f32_e32 v96, v97, v96
	v_add_f32_e32 v100, v100, v96
	ds_read_b128 v[162:165], v34 offset:60416
	s_waitcnt lgkmcnt(7)
	v_mul_f32_e32 v93, v167, v57
	v_fmac_f32_e32 v93, v166, v56
	v_mul_f32_e32 v92, v169, v63
	v_fmac_f32_e32 v92, v168, v62
	v_add_f32_e32 v92, v93, v92
	s_waitcnt lgkmcnt(6)
	v_mul_f32_e32 v97, v171, v61
	v_add_f32_e32 v100, v100, v92
	v_fmac_f32_e32 v97, v170, v60
	v_mul_f32_e32 v96, v173, v67
	ds_read_b128 v[166:169], v34 offset:61440
	v_fmac_f32_e32 v96, v172, v66
	v_add_f32_e32 v96, v97, v96
	v_add_f32_e32 v100, v100, v96
	ds_read_b128 v[170:173], v34 offset:62464
	s_waitcnt lgkmcnt(7)
	v_mul_f32_e32 v93, v175, v65
	v_fmac_f32_e32 v93, v174, v64
	v_mul_f32_e32 v92, v177, v71
	v_fmac_f32_e32 v92, v176, v70
	v_add_f32_e32 v92, v93, v92
	s_waitcnt lgkmcnt(6)
	v_mul_f32_e32 v93, v179, v69
	v_mul_f32_e32 v94, v181, v73
	v_fmac_f32_e32 v93, v178, v68
	v_fmac_f32_e32 v94, v180, v72
	v_add_f32_e32 v92, v100, v92
	v_add_f32_e32 v93, v93, v94
	v_add_f32_e32 v92, v92, v93
	s_nop 1
	v_add_f32_dpp v92, v92, v92 quad_perm:[1,0,3,2] row_mask:0xf bank_mask:0xf bound_ctrl:1
	s_nop 1
	v_add_f32_dpp v92, v92, v92 quad_perm:[2,3,0,1] row_mask:0xf bank_mask:0xf bound_ctrl:1
	s_nop 1
	v_add_f32_dpp v92, v92, v92 row_half_mirror row_mask:0xf bank_mask:0xf bound_ctrl:1
	s_nop 1
	v_add_f32_dpp v96, v92, v92 row_mirror row_mask:0xf bank_mask:0xf bound_ctrl:1
	ds_read_b128 v[174:177], v34 offset:63488
	v_readlane_b32 s20, v96, 0
	v_readlane_b32 s73, v96, 16
	v_readlane_b32 s21, v96, 32
	v_readlane_b32 s74, v96, 48
	ds_read_b128 v[178:181], v34 offset:64512
	s_waitcnt lgkmcnt(7)
	v_mul_f32_e32 v93, v151, v43
	v_fmac_f32_e32 v93, v150, v42
	v_mul_f32_e32 v92, v153, v47
	v_fmac_f32_e32 v92, v152, v46
	v_add_f32_e32 v92, v93, v92
	s_waitcnt lgkmcnt(6)
	v_mul_f32_e32 v97, v155, v45
	v_add_f32_e32 v100, 0, v92
	v_fmac_f32_e32 v97, v154, v44
	v_mul_f32_e32 v96, v157, v51
	v_fmac_f32_e32 v96, v156, v50
	v_add_f32_e32 v96, v97, v96
	v_add_f32_e32 v100, v100, v96
	s_waitcnt lgkmcnt(5)
	v_mul_f32_e32 v93, v159, v49
	v_fmac_f32_e32 v93, v158, v48
	v_mul_f32_e32 v92, v161, v55
	v_fmac_f32_e32 v92, v160, v54
	v_add_f32_e32 v92, v93, v92
	s_waitcnt lgkmcnt(4)
	v_mul_f32_e32 v97, v163, v53
	v_add_f32_e32 v100, v100, v92
	v_fmac_f32_e32 v97, v162, v52
	v_mul_f32_e32 v96, v165, v59
	v_fmac_f32_e32 v96, v164, v58
	v_add_f32_e32 v96, v97, v96
	v_add_f32_e32 v100, v100, v96
	s_waitcnt lgkmcnt(3)
	v_mul_f32_e32 v93, v167, v57
	v_fmac_f32_e32 v93, v166, v56
	v_mul_f32_e32 v92, v169, v63
	v_fmac_f32_e32 v92, v168, v62
	v_add_f32_e32 v92, v93, v92
	s_waitcnt lgkmcnt(2)
	v_mul_f32_e32 v97, v171, v61
	v_add_f32_e32 v100, v100, v92
	v_fmac_f32_e32 v97, v170, v60
	v_mul_f32_e32 v96, v173, v67
	v_fmac_f32_e32 v96, v172, v66
	v_add_f32_e32 v96, v97, v96
	v_add_f32_e32 v100, v100, v96
	s_waitcnt lgkmcnt(1)
	v_mul_f32_e32 v93, v175, v65
	v_fmac_f32_e32 v93, v174, v64
	v_mul_f32_e32 v92, v177, v71
	v_fmac_f32_e32 v92, v176, v70
	v_add_f32_e32 v92, v93, v92
	s_waitcnt lgkmcnt(0)
	v_mul_f32_e32 v93, v179, v69
	v_mul_f32_e32 v94, v181, v73
	v_fmac_f32_e32 v93, v178, v68
	v_fmac_f32_e32 v94, v180, v72
	v_add_f32_e32 v92, v100, v92
	v_add_f32_e32 v93, v93, v94
	v_add_f32_e32 v92, v92, v93
	s_nop 1
	v_add_f32_dpp v92, v92, v92 quad_perm:[1,0,3,2] row_mask:0xf bank_mask:0xf bound_ctrl:1
	s_nop 1
	v_add_f32_dpp v92, v92, v92 quad_perm:[2,3,0,1] row_mask:0xf bank_mask:0xf bound_ctrl:1
	s_nop 1
	v_add_f32_dpp v92, v92, v92 row_half_mirror row_mask:0xf bank_mask:0xf bound_ctrl:1
	s_nop 1
	v_add_f32_dpp v92, v92, v92 row_mirror row_mask:0xf bank_mask:0xf bound_ctrl:1
	s_nop 0
	v_readlane_b32 s50, v92, 0
	v_readlane_b32 s75, v92, 16
	v_readlane_b32 s51, v92, 32
	v_readlane_b32 s76, v92, 48
	s_and_saveexec_b64 s[46:47], s[4:5]
	s_cbranch_execz .LBB0_1381
	v_readlane_b32 s80, v251, 0
	v_readlane_b32 s82, v251, 2
	v_readlane_b32 s83, v251, 3
	s_nop 4
	v_mov_b32_e32 v92, v234
	v_mov_b32_e32 v93, v235
	v_mov_b32_e32 v94, v236
	v_mov_b32_e32 v95, v237
	v_mov_b32_e32 v96, v238
	v_mov_b32_e32 v97, v239
	v_mov_b32_e32 v98, v240
	v_mov_b32_e32 v99, v241
	v_mov_b32_e32 v100, s75
	v_mov_b32_e32 v101, s76
	v_mov_b32_e32 v120, s53
	v_mov_b32_e32 v121, s63
	v_mov_b32_e32 v122, s39
	v_mov_b32_e32 v123, s52
	v_mov_b32_e32 v102, s73
	v_mov_b32_e32 v103, s74
	v_mov_b32_e32 v104, s71
	v_mov_b32_e32 v105, s72
	v_mov_b32_e32 v106, s69
	v_mov_b32_e32 v107, s70
	v_pk_add_f32 v[100:101], s[50:51], v[100:101]
	v_pk_add_f32 v[120:121], s[6:7], v[120:121]
	v_pk_add_f32 v[122:123], s[0:1], v[122:123]
	v_pk_add_f32 v[102:103], s[20:21], v[102:103]
	v_pk_add_f32 v[104:105], s[18:19], v[104:105]
	v_pk_add_f32 v[106:107], s[16:17], v[106:107]
	v_add_f32_e32 v117, v100, v101
	v_mov_b32_e32 v100, v122
	v_mov_b32_e32 v101, v120
	v_mov_b32_e32 v120, v123
	v_mov_b32_e32 v118, s64
	v_mov_b32_e32 v119, s65
	v_add_f32_e32 v102, v102, v103
	v_add_f32_e32 v103, v104, v105
	v_add_f32_e32 v104, v106, v107
	v_pk_add_f32 v[100:101], v[100:101], v[120:121]
	v_pk_add_f32 v[118:119], s[8:9], v[118:119]
	v_mov_b32_e32 v108, s66
	v_mov_b32_e32 v109, s67
	v_add_f32_e32 v106, v118, v119
	v_pk_add_f32 v[108:109], s[14:15], v[108:109]
	s_mov_b64 s[48:49], exec
	v_add_f32_e32 v105, v108, v109
	v_readlane_b32 s81, v251, 1
	v_readlane_b32 s84, v251, 4
	v_readlane_b32 s85, v251, 5
	v_readlane_b32 s86, v251, 6
	v_readlane_b32 s87, v251, 7
	s_waitcnt vmcnt(0)
	v_add_f32_e32 v94, v94, v102
	v_add_f32_e32 v102, v93, v103
	v_add_f32_e32 v103, v92, v104
	v_pk_add_f32 v[92:93], v[96:97], v[100:101]
	v_add_f32_e32 v98, v98, v106
	v_cmp_gt_f32_e32 vcc, v93, v92
	v_add_f32_e32 v99, v99, v105
	v_add_f32_e32 v95, v95, v117
	v_cndmask_b32_e32 v96, v92, v93, vcc
	v_cmp_gt_f32_e64 s[6:7], v98, v96
	v_cndmask_b32_e64 v97, 0, 1, vcc
	v_cmp_nlt_f32_e64 s[0:1], s62, v92
	v_cndmask_b32_e64 v96, v96, v98, s[6:7]
	v_cmp_gt_f32_e32 vcc, v99, v96
	v_readfirstlane_b32 s39, v97
	s_nop 0
	v_cndmask_b32_e32 v96, v96, v99, vcc
	v_cmp_gt_f32_e64 s[8:9], v103, v96
	s_nop 1
	v_cndmask_b32_e64 v96, v96, v103, s[8:9]
	v_cmp_gt_f32_e64 s[14:15], v102, v96
	s_nop 1
	v_cndmask_b32_e64 v96, v96, v102, s[14:15]
	v_cmp_gt_f32_e64 s[16:17], v94, v96
	s_nop 1
	v_cndmask_b32_e64 v96, v96, v94, s[16:17]
	v_cmp_ngt_f32_e64 s[18:19], v95, v96
	s_and_b64 s[20:21], s[18:19], s[16:17]
	s_and_b64 s[6:7], s[6:7], exec
	s_cselect_b32 s39, 2, s39
	s_and_b64 s[6:7], vcc, exec
	s_cselect_b32 s39, 3, s39
	s_and_b64 s[6:7], s[8:9], exec
	s_cselect_b32 s8, 4, s39
	s_and_b64 s[6:7], s[14:15], exec
	s_cselect_b32 s8, 5, s8
	s_and_b64 s[6:7], s[16:17], exec
	s_cselect_b32 s8, 6, s8
	s_and_b64 s[6:7], s[18:19], exec
	s_cselect_b32 s39, s8, 7
	s_cmp_lg_u32 s39, 5
	s_cselect_b64 s[16:17], -1, 0
	s_cmp_lg_u32 s39, 4
	s_cselect_b64 s[14:15], -1, 0
	s_cmp_lg_u32 s39, 3
	s_cselect_b64 s[8:9], -1, 0
	s_cmp_lg_u32 s39, 2
	s_cselect_b64 s[6:7], -1, 0
	s_cmp_lg_u32 s39, 1
	s_cselect_b64 s[50:51], -1, 0
	s_cmp_eq_u32 s39, 0
	s_cselect_b64 s[52:53], -1, 0
	s_or_b64 vcc, s[52:53], s[0:1]
	v_cndmask_b32_e32 v92, v92, v116, vcc
	v_cmp_gt_f32_e64 s[0:1], v93, v92
	v_cndmask_b32_e64 v97, 0, -1, vcc
	s_and_b64 vcc, s[50:51], s[0:1]
	v_cndmask_b32_e32 v92, v92, v93, vcc
	v_cmp_gt_f32_e64 s[0:1], v98, v92
	s_and_b64 s[0:1], s[6:7], s[0:1]
	v_cndmask_b32_e64 v96, v95, v96, s[18:19]
	v_cndmask_b32_e64 v92, v92, v98, s[0:1]
	v_cmp_gt_f32_e64 s[6:7], v99, v92
	s_and_b64 s[6:7], s[8:9], s[6:7]
	v_readfirstlane_b32 s50, v97
	v_cndmask_b32_e64 v92, v92, v99, s[6:7]
	v_cmp_gt_f32_e64 s[8:9], v103, v92
	s_and_b64 s[8:9], s[14:15], s[8:9]
	s_nop 0
	v_cndmask_b32_e64 v92, v92, v103, s[8:9]
	v_cmp_gt_f32_e64 s[14:15], v102, v92
	s_and_b64 s[14:15], s[16:17], s[14:15]
	s_nop 0
	v_cndmask_b32_e64 v92, v92, v102, s[14:15]
	v_cmp_ngt_f32_e64 s[16:17], v94, v92
	s_or_b64 s[16:17], s[20:21], s[16:17]
	s_nop 0
	v_cndmask_b32_e64 v92, v94, v92, s[16:17]
	v_cmp_gt_f32_e64 s[20:21], v95, v92
	s_and_b64 s[18:19], s[18:19], s[20:21]
	v_cndmask_b32_e64 v92, v92, v95, s[18:19]
	v_sub_f32_e32 v92, v92, v96
	v_mul_f32_e32 v92, 0x3fb8aa3b, v92
	v_exp_f32_e32 v92, v92
	s_and_b64 s[20:21], vcc, exec
	s_cselect_b32 s20, 1, s50
	s_and_b64 s[0:1], s[0:1], exec
	v_add_f32_e32 v92, 1.0, v92
	v_div_scale_f32 v93, s[0:1], v92, v92, 1.0
	v_rcp_f32_e32 v94, v93
	s_cselect_b32 s20, 2, s20
	s_and_b64 s[0:1], s[6:7], exec
	s_cselect_b32 s6, 3, s20
	s_and_b64 s[0:1], s[8:9], exec
	s_cselect_b32 s6, 4, s6
	s_and_b64 s[0:1], s[14:15], exec
	s_cselect_b32 s6, 5, s6
	s_and_b64 s[0:1], s[16:17], exec
	v_fma_f32 v95, -v93, v94, 1.0
	s_cselect_b32 s6, s6, 6
	s_and_b64 s[0:1], s[18:19], exec
	v_fmac_f32_e32 v94, v95, v94
	v_div_scale_f32 v95, vcc, 1.0, v92, 1.0
	s_cselect_b32 s6, 7, s6
	v_mul_f32_e32 v96, v95, v94
	v_fma_f32 v97, -v93, v96, v95
	s_lshl_b32 s0, s6, 8
	v_fmac_f32_e32 v96, v97, v94
	s_add_i32 s7, s0, s39
	v_fma_f32 v93, -v93, v96, v95
	s_add_u32 s0, s56, s28
	v_div_fmas_f32 v93, v93, v94, v96
	s_addc_u32 s1, s57, s29
	v_mov_b32_e32 v94, s7
	v_div_fixup_f32 v92, v93, v92, 1.0
	global_store_dword v113, v94, s[0:1]
	s_add_u32 s0, s56, s42
	v_sub_f32_e32 v93, 1.0, v92
	s_addc_u32 s1, s57, s43
	global_store_dwordx2 v114, v[92:93], s[0:1]
	v_mbcnt_lo_u32_b32 v92, s48, 0
	v_mbcnt_hi_u32_b32 v92, s49, v92
	v_cmp_eq_u32_e32 vcc, 0, v92
	s_and_saveexec_b64 s[0:1], vcc
	s_cbranch_execz .LBB0_1379
	s_lshl_b32 s7, s39, 2
	s_add_i32 s7, s7, 0
	s_add_i32 s7, s7, 0x10000
	s_bcnt1_i32_b64 s8, s[48:49]
	v_mov_b32_e32 v92, s7
	v_mov_b32_e32 v93, s8
	ds_add_u32 v92, v93

.LBB0_1383:
	s_waitcnt vmcnt(15)
	v_lshlrev_b32_e32 v92, 16, v90
	v_and_b32_e32 v93, 0xffff0000, v90
	v_lshlrev_b32_e32 v90, 16, v91
	v_and_b32_e32 v91, 0xffff0000, v91
	s_waitcnt vmcnt(14)
	v_lshlrev_b32_e32 v95, 16, v89
	v_lshlrev_b32_e32 v94, 16, v88
	v_and_b32_e32 v89, 0xffff0000, v89
	v_and_b32_e32 v88, 0xffff0000, v88
	s_waitcnt vmcnt(12)
	v_lshlrev_b32_e32 v119, 16, v80
	v_and_b32_e32 v121, 0xffff0000, v80
	s_waitcnt vmcnt(8)
	v_lshlrev_b32_e32 v109, 16, v76
	v_and_b32_e32 v107, 0xffff0000, v76
	v_mul_f32_e32 v76, v91, v91
	v_mul_f32_e32 v80, v93, v93
	v_lshlrev_b32_e32 v122, 16, v81
	v_and_b32_e32 v123, 0xffff0000, v81
	v_lshlrev_b32_e32 v96, 16, v78
	v_and_b32_e32 v97, 0xffff0000, v78
	v_lshlrev_b32_e32 v102, 16, v79
	v_and_b32_e32 v103, 0xffff0000, v79
	v_lshlrev_b32_e32 v104, 16, v77
	v_and_b32_e32 v105, 0xffff0000, v77
	v_pk_fma_f32 v[76:77], v[90:91], v[90:91], v[76:77] op_sel_hi:[1,1,0]
	v_pk_mul_f32 v[78:79], v[88:89], v[88:89]
	v_pk_fma_f32 v[80:81], v[92:93], v[92:93], v[80:81] op_sel_hi:[1,1,0]
	v_lshlrev_b32_e32 v98, 16, v82
	v_and_b32_e32 v99, 0xffff0000, v82
	v_lshlrev_b32_e32 v100, 16, v83
	v_and_b32_e32 v101, 0xffff0000, v83
	v_pk_fma_f32 v[78:79], v[94:95], v[94:95], v[78:79]
	v_mov_b32_e32 v118, v80
	v_mov_b32_e32 v82, v76
	v_mov_b32_e32 v83, v119
	v_lshlrev_b32_e32 v128, 16, v84
	v_and_b32_e32 v130, 0xffff0000, v84
	v_mul_f32_e32 v84, v121, v121
	v_pk_add_f32 v[76:77], v[80:81], v[76:77]
	v_pk_mul_f32 v[80:81], v[118:119], v[82:83]
	v_pk_add_f32 v[78:79], v[78:79], v[78:79] op_sel:[0,1] op_sel_hi:[1,0]
	v_mov_b32_e32 v77, v81
	v_mov_b32_e32 v79, v84
	v_pk_add_f32 v[76:77], v[76:77], v[78:79]
	v_mul_f32_e32 v78, v99, v99
	v_mul_f32_e32 v80, v101, v101
	v_lshlrev_b32_e32 v124, 16, v86
	v_and_b32_e32 v126, 0xffff0000, v86
	v_lshlrev_b32_e32 v129, 16, v85
	v_and_b32_e32 v131, 0xffff0000, v85
	v_mul_f32_e32 v85, v122, v122
	v_mul_f32_e32 v86, v123, v123
	v_pk_fma_f32 v[78:79], v[98:99], v[98:99], v[78:79] op_sel_hi:[1,1,0]
	v_pk_fma_f32 v[80:81], v[100:101], v[100:101], v[80:81] op_sel_hi:[1,1,0]
	v_mov_b32_e32 v79, v85
	v_mov_b32_e32 v81, v86
	v_and_b32_e32 v127, 0xffff0000, v87
	v_pk_add_f32 v[78:79], v[78:79], v[80:81]
	v_lshlrev_b32_e32 v125, 16, v87
	v_pk_add_f32 v[76:77], v[76:77], v[78:79]
	v_pk_mul_f32 v[78:79], v[126:127], v[126:127]
	v_pk_add_f32 v[76:77], v[76:77], v[76:77] op_sel:[0,1] op_sel_hi:[1,0]
	v_pk_fma_f32 v[78:79], v[124:125], v[124:125], v[78:79]
	v_pk_mul_f32 v[80:81], v[130:131], v[130:131]
	v_pk_add_f32 v[78:79], v[78:79], v[78:79] op_sel:[0,1] op_sel_hi:[1,0]
	v_mov_b32_e32 v108, v76
	v_mov_b32_e32 v82, v78
	v_mov_b32_e32 v83, v109
	v_pk_fma_f32 v[80:81], v[128:129], v[128:129], v[80:81]
	v_pk_add_f32 v[76:77], v[76:77], v[78:79]
	v_pk_mul_f32 v[78:79], v[108:109], v[82:83]
	v_mul_f32_e32 v84, v107, v107
	v_mov_b32_e32 v77, v79
	v_pk_add_f32 v[78:79], v[80:81], v[80:81] op_sel:[0,1] op_sel_hi:[1,0]
	v_mul_f32_e32 v80, v103, v103
	v_mov_b32_e32 v79, v84
	v_pk_add_f32 v[76:77], v[76:77], v[78:79]
	v_mul_f32_e32 v78, v97, v97
	v_mul_f32_e32 v85, v104, v104
	v_mul_f32_e32 v86, v105, v105
	v_pk_fma_f32 v[78:79], v[96:97], v[96:97], v[78:79] op_sel_hi:[1,1,0]
	v_pk_fma_f32 v[80:81], v[102:103], v[102:103], v[80:81] op_sel_hi:[1,1,0]
	v_mov_b32_e32 v79, v85
	v_mov_b32_e32 v81, v86
	v_pk_add_f32 v[78:79], v[78:79], v[80:81]
	v_mov_b32_e32 v82, 0
	v_pk_add_f32 v[76:77], v[76:77], v[78:79]
	v_mov_b32_e32 v106, 0
	v_add_f32_e32 v76, v76, v77
	v_mov_b32_e32 v120, v119
	v_mov_b32_e32 v117, 0
	v_add_f32_dpp v76, v76, v76 quad_perm:[1,0,3,2] row_mask:0xf bank_mask:0xf bound_ctrl:1
	s_nop 1
	v_add_f32_dpp v76, v76, v76 quad_perm:[2,3,0,1] row_mask:0xf bank_mask:0xf bound_ctrl:1
	s_nop 1
	v_add_f32_dpp v76, v76, v76 row_half_mirror row_mask:0xf bank_mask:0xf bound_ctrl:1
	s_nop 1
	v_add_f32_dpp v76, v76, v76 row_mirror row_mask:0xf bank_mask:0xf bound_ctrl:1
	s_nop 0
	v_readlane_b32 s6, v76, 16
	v_readlane_b32 s7, v76, 48
	v_readlane_b32 s0, v76, 0
	v_readlane_b32 s1, v76, 32
	v_mov_b32_e32 v76, s6
	v_mov_b32_e32 v77, s7
	v_pk_add_f32 v[76:77], s[0:1], v[76:77]
	s_nop 0
	v_add_f32_e32 v76, v76, v77
	v_fmamk_f32 v76, v76, 0x3a000000, v111
	v_mul_f32_e32 v77, 0x4f800000, v76
	v_cmp_gt_f32_e32 vcc, s35, v76
	s_nop 1
	v_cndmask_b32_e32 v76, v76, v77, vcc
	v_sqrt_f32_e32 v77, v76
	s_nop 0
	v_add_u32_e32 v78, -1, v77
	v_fma_f32 v79, -v78, v77, v76
	v_cmp_ge_f32_e64 s[0:1], 0, v79
	v_add_u32_e32 v79, 1, v77
	s_nop 0
	v_cndmask_b32_e64 v78, v77, v78, s[0:1]
	v_fma_f32 v77, -v79, v77, v76
	v_cmp_lt_f32_e64 s[0:1], 0, v77
	s_nop 1
	v_cndmask_b32_e64 v77, v78, v79, s[0:1]
	v_mul_f32_e32 v78, 0x37800000, v77
	v_cndmask_b32_e32 v77, v77, v78, vcc
	v_cmp_class_f32_e32 vcc, v76, v112
	s_nop 1
	v_cndmask_b32_e32 v76, v77, v76, vcc
	v_div_scale_f32 v77, s[0:1], v76, v76, 1.0
	v_rcp_f32_e32 v78, v77
	s_nop 0
	v_fma_f32 v79, -v77, v78, 1.0
	v_fmac_f32_e32 v78, v79, v78
	v_div_scale_f32 v79, vcc, 1.0, v76, 1.0
	v_mul_f32_e32 v80, v79, v78
	v_fma_f32 v81, -v77, v80, v79
	v_fmac_f32_e32 v80, v81, v78
	v_fma_f32 v77, -v77, v80, v79
	v_div_fmas_f32 v77, v77, v78, v80
	v_div_fixup_f32 v108, v77, v76, 1.0
	v_pk_mul_f32 v[76:77], v[108:109], v[92:93] op_sel_hi:[0,1]
	v_pk_mul_f32 v[76:77], v[76:77], v[14:15]
	v_pk_mul_f32 v[78:79], v[108:109], v[90:91] op_sel_hi:[0,1]
	v_med3_f32 v80, v76, s60, v115
	v_med3_f32 v81, v77, s60, v115
	v_cvt_pk_fp8_f32 v82, v80, v81
	v_pk_mul_f32 v[78:79], v[78:79], v[16:17]
	v_pk_mul_f32 v[86:87], v[108:109], v[100:101] op_sel_hi:[0,1]
	v_med3_f32 v80, v78, s60, v115
	v_med3_f32 v81, v79, s60, v115
	v_cvt_pk_fp8_f32 v82, v80, v81 op_sel:[0,0,1]
	v_mov_b32_e32 v80, v94
	v_mov_b32_e32 v81, v88
	v_pk_mul_f32 v[80:81], v[108:109], v[80:81] op_sel_hi:[0,1]
	v_pk_mul_f32 v[84:85], v[80:81], v[2:3]
	v_mov_b32_e32 v88, v95
	v_med3_f32 v80, v84, s60, v115
	v_med3_f32 v81, v85, s60, v115
	v_cvt_pk_fp8_f32 v106, v80, v81
	global_store_dword v[74:75], v82, off offset:2048
	v_pk_mul_f32 v[82:83], v[108:109], v[88:89] op_sel_hi:[0,1]
	v_pk_mul_f32 v[82:83], v[82:83], v[4:5]
	v_pk_mul_f32 v[86:87], v[86:87], v[8:9]
	v_med3_f32 v80, v82, s60, v115
	v_med3_f32 v81, v83, s60, v115
	v_cvt_pk_fp8_f32 v106, v80, v81 op_sel:[0,0,1]
	v_pk_mul_f32 v[80:81], v[108:109], v[98:99] op_sel_hi:[0,1]
	v_pk_mul_f32 v[80:81], v[80:81], v[6:7]
	v_mov_b32_e32 v98, 0
	v_med3_f32 v88, v80, s60, v115
	v_med3_f32 v89, v81, s60, v115
	v_cvt_pk_fp8_f32 v98, v88, v89
	v_med3_f32 v88, v86, s60, v115
	v_med3_f32 v89, v87, s60, v115
	v_mov_b32_e32 v99, 0
	v_cvt_pk_fp8_f32 v98, v88, v89 op_sel:[0,0,1]
	v_pk_mul_f32 v[88:89], v[108:109], v[120:121] op_sel_hi:[0,1]
	v_pk_mul_f32 v[90:91], v[88:89], v[10:11]
	v_pk_mul_f32 v[92:93], v[108:109], v[122:123] op_sel_hi:[0,1]
	v_med3_f32 v88, v90, s60, v115
	v_med3_f32 v89, v91, s60, v115
	v_cvt_pk_fp8_f32 v99, v88, v89
	v_pk_mul_f32 v[88:89], v[92:93], v[12:13]
	v_pk_mul_f32 v[96:97], v[108:109], v[96:97] op_sel_hi:[0,1]
	v_med3_f32 v92, v88, s60, v115
	v_med3_f32 v93, v89, s60, v115
	v_cvt_pk_fp8_f32 v99, v92, v93 op_sel:[0,0,1]
	v_mov_b32_e32 v92, v124
	v_mov_b32_e32 v93, v126
	v_pk_mul_f32 v[92:93], v[108:109], v[92:93] op_sel_hi:[0,1]
	v_pk_mul_f32 v[92:93], v[92:93], v[18:19]
	v_mov_b32_e32 v126, v125
	v_med3_f32 v100, v92, s60, v115
	v_med3_f32 v101, v93, s60, v115
	v_cvt_pk_fp8_f32 v117, v100, v101
	v_pk_mul_f32 v[94:95], v[108:109], v[126:127] op_sel_hi:[0,1]
	v_pk_mul_f32 v[94:95], v[94:95], v[20:21]
	v_pk_mul_f32 v[96:97], v[96:97], v[26:27]
	v_med3_f32 v100, v94, s60, v115
	v_med3_f32 v101, v95, s60, v115
	v_cvt_pk_fp8_f32 v117, v100, v101 op_sel:[0,0,1]
	global_store_dword v[74:75], v106, off offset:2304
	global_store_dword v[74:75], v98, off offset:2560
	global_store_dword v[74:75], v99, off offset:2816
	global_store_dword v[74:75], v117, off offset:3072
	v_mov_b32_e32 v98, v128
	v_mov_b32_e32 v99, v130
	v_pk_mul_f32 v[98:99], v[108:109], v[98:99] op_sel_hi:[0,1]
	v_pk_mul_f32 v[100:101], v[98:99], v[22:23]
	v_mov_b32_e32 v117, 0
	v_med3_f32 v98, v100, s60, v115
	v_med3_f32 v99, v101, s60, v115
	v_mov_b32_e32 v130, v129
	v_cvt_pk_fp8_f32 v117, v98, v99
	v_pk_mul_f32 v[118:119], v[108:109], v[130:131] op_sel_hi:[0,1]
	v_pk_mul_f32 v[98:99], v[118:119], v[24:25]
	v_mov_b32_e32 v122, 0
	v_med3_f32 v106, v98, s60, v115
	v_med3_f32 v118, v99, s60, v115
	v_cvt_pk_fp8_f32 v117, v106, v118 op_sel:[0,0,1]
	v_med3_f32 v106, v96, s60, v115
	v_med3_f32 v118, v97, s60, v115
	v_cvt_pk_fp8_f32 v122, v106, v118
	v_pk_mul_f32 v[102:103], v[108:109], v[102:103] op_sel_hi:[0,1]
	v_pk_mul_f32 v[102:103], v[102:103], v[28:29]
	v_mov_b32_e32 v123, 0
	v_med3_f32 v106, v102, s60, v115
	v_med3_f32 v118, v103, s60, v115
	v_cvt_pk_fp8_f32 v122, v106, v118 op_sel:[0,0,1]
	v_mov_b32_e32 v106, v109
	v_pk_mul_f32 v[106:107], v[108:109], v[106:107] op_sel_hi:[0,1]
	v_pk_mul_f32 v[108:109], v[108:109], v[104:105] op_sel_hi:[0,1]
	v_pk_mul_f32 v[104:105], v[106:107], v[30:31]
	ds_read_b128 v[150:153], v34 offset:0
	ds_read_b128 v[154:157], v34 offset:1024
	ds_read_b128 v[158:161], v34 offset:2048
	ds_read_b128 v[162:165], v34 offset:3072
	ds_read_b128 v[166:169], v34 offset:4096
	ds_read_b128 v[170:173], v34 offset:5120
	ds_read_b128 v[174:177], v34 offset:6144
	v_med3_f32 v106, v104, s60, v115
	v_med3_f32 v107, v105, s60, v115
	v_cvt_pk_fp8_f32 v123, v106, v107
	v_pk_mul_f32 v[106:107], v[108:109], v[32:33]
	s_nop 0
	v_med3_f32 v108, v106, s60, v115
	v_med3_f32 v109, v107, s60, v115
	v_cvt_pk_fp8_f32 v123, v108, v109 op_sel:[0,0,1]
	global_store_dword v[74:75], v117, off offset:3328
	global_store_dword v[74:75], v122, off offset:3584
	global_store_dword v[74:75], v123, off offset:3840
	ds_read_b128 v[178:181], v34 offset:7168
	s_waitcnt lgkmcnt(7)
	v_mul_f32_e32 v74, v151, v77
	v_mul_f32_e32 v75, v153, v79
	v_fmac_f32_e32 v74, v150, v76
	v_fmac_f32_e32 v75, v152, v78
	ds_read_b128 v[150:153], v34 offset:8192
	v_add_f32_e32 v74, v74, v75
	s_waitcnt lgkmcnt(7)
	v_mul_f32_e32 v75, v155, v85
	v_mul_f32_e32 v108, v157, v83
	v_fmac_f32_e32 v75, v154, v84
	v_fmac_f32_e32 v108, v156, v82
	ds_read_b128 v[154:157], v34 offset:9216
	v_add_f32_e32 v74, 0, v74
	v_add_f32_e32 v75, v75, v108
	v_add_f32_e32 v74, v74, v75
	s_waitcnt lgkmcnt(7)
	v_mul_f32_e32 v75, v159, v81
	v_mul_f32_e32 v108, v161, v87
	v_fmac_f32_e32 v75, v158, v80
	v_fmac_f32_e32 v108, v160, v86
	ds_read_b128 v[158:161], v34 offset:10240
	v_add_f32_e32 v75, v75, v108
	v_add_f32_e32 v74, v74, v75
	s_waitcnt lgkmcnt(7)
	v_mul_f32_e32 v75, v163, v91
	v_mul_f32_e32 v108, v165, v89
	v_fmac_f32_e32 v75, v162, v90
	v_fmac_f32_e32 v108, v164, v88
	ds_read_b128 v[162:165], v34 offset:11264
	v_add_f32_e32 v75, v75, v108
	v_add_f32_e32 v74, v74, v75
	s_waitcnt lgkmcnt(7)
	v_mul_f32_e32 v75, v167, v93
	v_mul_f32_e32 v108, v169, v95
	v_fmac_f32_e32 v75, v166, v92
	v_fmac_f32_e32 v108, v168, v94
	ds_read_b128 v[166:169], v34 offset:12288
	v_add_f32_e32 v75, v75, v108
	v_add_f32_e32 v74, v74, v75
	s_waitcnt lgkmcnt(7)
	v_mul_f32_e32 v75, v171, v101
	v_mul_f32_e32 v108, v173, v99
	v_fmac_f32_e32 v75, v170, v100
	v_fmac_f32_e32 v108, v172, v98
	ds_read_b128 v[170:173], v34 offset:13312
	v_add_f32_e32 v75, v75, v108
	v_add_f32_e32 v74, v74, v75
	s_waitcnt lgkmcnt(7)
	v_mul_f32_e32 v75, v175, v97
	v_mul_f32_e32 v108, v177, v103
	v_fmac_f32_e32 v75, v174, v96
	v_fmac_f32_e32 v108, v176, v102
	v_add_f32_e32 v75, v75, v108
	v_add_f32_e32 v74, v74, v75
	ds_read_b128 v[174:177], v34 offset:14336
	s_waitcnt lgkmcnt(7)
	v_mul_f32_e32 v75, v179, v105
	v_mul_f32_e32 v108, v181, v107
	v_fmac_f32_e32 v75, v178, v104
	v_fmac_f32_e32 v108, v180, v106
	v_add_f32_e32 v75, v75, v108
	v_add_f32_e32 v74, v74, v75
	ds_read_b128 v[178:181], v34 offset:15360
	s_waitcnt lgkmcnt(7)
	v_mul_f32_e32 v75, v153, v79
	v_add_f32_dpp v74, v74, v74 quad_perm:[1,0,3,2] row_mask:0xf bank_mask:0xf bound_ctrl:1
	v_fmac_f32_e32 v75, v152, v78
	s_nop 0
	v_add_f32_dpp v74, v74, v74 quad_perm:[2,3,0,1] row_mask:0xf bank_mask:0xf bound_ctrl:1
	s_nop 1
	v_add_f32_dpp v74, v74, v74 row_half_mirror row_mask:0xf bank_mask:0xf bound_ctrl:1
	s_nop 1
	v_add_f32_dpp v74, v74, v74 row_mirror row_mask:0xf bank_mask:0xf bound_ctrl:1
	s_nop 0
	v_readlane_b32 s0, v74, 0
	v_readlane_b32 s39, v74, 16
	v_readlane_b32 s1, v74, 32
	v_readlane_b32 s63, v74, 48
	v_mul_f32_e32 v74, v151, v77
	v_fmac_f32_e32 v74, v150, v76
	ds_read_b128 v[150:153], v34 offset:16384
	v_add_f32_e32 v74, v74, v75
	s_waitcnt lgkmcnt(7)
	v_mul_f32_e32 v75, v155, v85
	v_mul_f32_e32 v108, v157, v83
	v_fmac_f32_e32 v75, v154, v84
	v_fmac_f32_e32 v108, v156, v82
	ds_read_b128 v[154:157], v34 offset:17408
	v_add_f32_e32 v74, 0, v74
	v_add_f32_e32 v75, v75, v108
	v_add_f32_e32 v74, v74, v75
	s_waitcnt lgkmcnt(7)
	v_mul_f32_e32 v75, v159, v81
	v_mul_f32_e32 v108, v161, v87
	v_fmac_f32_e32 v75, v158, v80
	v_fmac_f32_e32 v108, v160, v86
	ds_read_b128 v[158:161], v34 offset:18432
	v_add_f32_e32 v75, v75, v108
	v_add_f32_e32 v74, v74, v75
	s_waitcnt lgkmcnt(7)
	v_mul_f32_e32 v75, v163, v91
	v_mul_f32_e32 v108, v165, v89
	v_fmac_f32_e32 v75, v162, v90
	v_fmac_f32_e32 v108, v164, v88
	ds_read_b128 v[162:165], v34 offset:19456
	v_add_f32_e32 v75, v75, v108
	v_add_f32_e32 v74, v74, v75
	s_waitcnt lgkmcnt(7)
	v_mul_f32_e32 v75, v167, v93
	v_mul_f32_e32 v108, v169, v95
	v_fmac_f32_e32 v75, v166, v92
	v_fmac_f32_e32 v108, v168, v94
	ds_read_b128 v[166:169], v34 offset:20480
	v_add_f32_e32 v75, v75, v108
	v_add_f32_e32 v74, v74, v75
	s_waitcnt lgkmcnt(7)
	v_mul_f32_e32 v75, v171, v101
	v_mul_f32_e32 v108, v173, v99
	v_fmac_f32_e32 v75, v170, v100
	v_fmac_f32_e32 v108, v172, v98
	ds_read_b128 v[170:173], v34 offset:21504
	v_add_f32_e32 v75, v75, v108
	v_add_f32_e32 v74, v74, v75
	s_waitcnt lgkmcnt(7)
	v_mul_f32_e32 v75, v175, v97
	v_mul_f32_e32 v108, v177, v103
	v_fmac_f32_e32 v75, v174, v96
	v_fmac_f32_e32 v108, v176, v102
	v_add_f32_e32 v75, v75, v108
	v_add_f32_e32 v74, v74, v75
	ds_read_b128 v[174:177], v34 offset:22528
	s_waitcnt lgkmcnt(7)
	v_mul_f32_e32 v75, v179, v105
	v_mul_f32_e32 v108, v181, v107
	v_fmac_f32_e32 v75, v178, v104
	v_fmac_f32_e32 v108, v180, v106
	v_add_f32_e32 v75, v75, v108
	v_add_f32_e32 v74, v74, v75
	ds_read_b128 v[178:181], v34 offset:23552
	s_waitcnt lgkmcnt(7)
	v_mul_f32_e32 v75, v153, v79
	v_add_f32_dpp v74, v74, v74 quad_perm:[1,0,3,2] row_mask:0xf bank_mask:0xf bound_ctrl:1
	v_fmac_f32_e32 v75, v152, v78
	s_nop 0
	v_add_f32_dpp v74, v74, v74 quad_perm:[2,3,0,1] row_mask:0xf bank_mask:0xf bound_ctrl:1
	s_nop 1
	v_add_f32_dpp v74, v74, v74 row_half_mirror row_mask:0xf bank_mask:0xf bound_ctrl:1
	s_nop 1
	v_add_f32_dpp v74, v74, v74 row_mirror row_mask:0xf bank_mask:0xf bound_ctrl:1
	s_nop 0
	v_readlane_b32 s6, v74, 0
	v_readlane_b32 s64, v74, 16
	v_readlane_b32 s7, v74, 32
	v_readlane_b32 s65, v74, 48
	v_mul_f32_e32 v74, v151, v77
	v_fmac_f32_e32 v74, v150, v76
	ds_read_b128 v[150:153], v34 offset:24576
	v_add_f32_e32 v74, v74, v75
	s_waitcnt lgkmcnt(7)
	v_mul_f32_e32 v75, v155, v85
	v_mul_f32_e32 v108, v157, v83
	v_fmac_f32_e32 v75, v154, v84
	v_fmac_f32_e32 v108, v156, v82
	ds_read_b128 v[154:157], v34 offset:25600
	v_add_f32_e32 v74, 0, v74
	v_add_f32_e32 v75, v75, v108
	v_add_f32_e32 v74, v74, v75
	s_waitcnt lgkmcnt(7)
	v_mul_f32_e32 v75, v159, v81
	v_mul_f32_e32 v108, v161, v87
	v_fmac_f32_e32 v75, v158, v80
	v_fmac_f32_e32 v108, v160, v86
	ds_read_b128 v[158:161], v34 offset:26624
	v_add_f32_e32 v75, v75, v108
	v_add_f32_e32 v74, v74, v75
	s_waitcnt lgkmcnt(7)
	v_mul_f32_e32 v75, v163, v91
	v_mul_f32_e32 v108, v165, v89
	v_fmac_f32_e32 v75, v162, v90
	v_fmac_f32_e32 v108, v164, v88
	ds_read_b128 v[162:165], v34 offset:27648
	v_add_f32_e32 v75, v75, v108
	v_add_f32_e32 v74, v74, v75
	s_waitcnt lgkmcnt(7)
	v_mul_f32_e32 v75, v167, v93
	v_mul_f32_e32 v108, v169, v95
	v_fmac_f32_e32 v75, v166, v92
	v_fmac_f32_e32 v108, v168, v94
	ds_read_b128 v[166:169], v34 offset:28672
	v_add_f32_e32 v75, v75, v108
	v_add_f32_e32 v74, v74, v75
	s_waitcnt lgkmcnt(7)
	v_mul_f32_e32 v75, v171, v101
	v_mul_f32_e32 v108, v173, v99
	v_fmac_f32_e32 v75, v170, v100
	v_fmac_f32_e32 v108, v172, v98
	ds_read_b128 v[170:173], v34 offset:29696
	v_add_f32_e32 v75, v75, v108
	v_add_f32_e32 v74, v74, v75
	s_waitcnt lgkmcnt(7)
	v_mul_f32_e32 v75, v175, v97
	v_mul_f32_e32 v108, v177, v103
	v_fmac_f32_e32 v75, v174, v96
	v_fmac_f32_e32 v108, v176, v102
	v_add_f32_e32 v75, v75, v108
	v_add_f32_e32 v74, v74, v75
	ds_read_b128 v[174:177], v34 offset:30720
	s_waitcnt lgkmcnt(7)
	v_mul_f32_e32 v75, v179, v105
	v_mul_f32_e32 v108, v181, v107
	v_fmac_f32_e32 v75, v178, v104
	v_fmac_f32_e32 v108, v180, v106
	v_add_f32_e32 v75, v75, v108
	v_add_f32_e32 v74, v74, v75
	ds_read_b128 v[178:181], v34 offset:31744
	s_waitcnt lgkmcnt(7)
	v_mul_f32_e32 v75, v153, v79
	v_add_f32_dpp v74, v74, v74 quad_perm:[1,0,3,2] row_mask:0xf bank_mask:0xf bound_ctrl:1
	v_fmac_f32_e32 v75, v152, v78
	s_nop 0
	v_add_f32_dpp v74, v74, v74 quad_perm:[2,3,0,1] row_mask:0xf bank_mask:0xf bound_ctrl:1
	s_nop 1
	v_add_f32_dpp v74, v74, v74 row_half_mirror row_mask:0xf bank_mask:0xf bound_ctrl:1
	s_nop 1
	v_add_f32_dpp v74, v74, v74 row_mirror row_mask:0xf bank_mask:0xf bound_ctrl:1
	s_nop 0
	v_readlane_b32 s8, v74, 0
	v_readlane_b32 s66, v74, 16
	v_readlane_b32 s9, v74, 32
	v_readlane_b32 s67, v74, 48
	v_mul_f32_e32 v74, v151, v77
	v_fmac_f32_e32 v74, v150, v76
	ds_read_b128 v[150:153], v34 offset:32768
	v_add_f32_e32 v74, v74, v75
	s_waitcnt lgkmcnt(7)
	v_mul_f32_e32 v75, v155, v85
	v_mul_f32_e32 v108, v157, v83
	v_fmac_f32_e32 v75, v154, v84
	v_fmac_f32_e32 v108, v156, v82
	ds_read_b128 v[154:157], v34 offset:33792
	v_add_f32_e32 v74, 0, v74
	v_add_f32_e32 v75, v75, v108
	v_add_f32_e32 v74, v74, v75
	s_waitcnt lgkmcnt(7)
	v_mul_f32_e32 v75, v159, v81
	v_mul_f32_e32 v108, v161, v87
	v_fmac_f32_e32 v75, v158, v80
	v_fmac_f32_e32 v108, v160, v86
	ds_read_b128 v[158:161], v34 offset:34816
	v_add_f32_e32 v75, v75, v108
	v_add_f32_e32 v74, v74, v75
	s_waitcnt lgkmcnt(7)
	v_mul_f32_e32 v75, v163, v91
	v_mul_f32_e32 v108, v165, v89
	v_fmac_f32_e32 v75, v162, v90
	v_fmac_f32_e32 v108, v164, v88
	ds_read_b128 v[162:165], v34 offset:35840
	v_add_f32_e32 v75, v75, v108
	v_add_f32_e32 v74, v74, v75
	s_waitcnt lgkmcnt(7)
	v_mul_f32_e32 v75, v167, v93
	v_mul_f32_e32 v108, v169, v95
	v_fmac_f32_e32 v75, v166, v92
	v_fmac_f32_e32 v108, v168, v94
	ds_read_b128 v[166:169], v34 offset:36864
	v_add_f32_e32 v75, v75, v108
	v_add_f32_e32 v74, v74, v75
	s_waitcnt lgkmcnt(7)
	v_mul_f32_e32 v75, v171, v101
	v_mul_f32_e32 v108, v173, v99
	v_fmac_f32_e32 v75, v170, v100
	v_fmac_f32_e32 v108, v172, v98
	ds_read_b128 v[170:173], v34 offset:37888
	v_add_f32_e32 v75, v75, v108
	v_add_f32_e32 v74, v74, v75
	s_waitcnt lgkmcnt(7)
	v_mul_f32_e32 v75, v175, v97
	v_mul_f32_e32 v108, v177, v103
	v_fmac_f32_e32 v75, v174, v96
	v_fmac_f32_e32 v108, v176, v102
	v_add_f32_e32 v75, v75, v108
	v_add_f32_e32 v74, v74, v75
	s_waitcnt lgkmcnt(6)
	v_mul_f32_e32 v75, v179, v105
	v_mul_f32_e32 v108, v181, v107
	v_fmac_f32_e32 v75, v178, v104
	v_fmac_f32_e32 v108, v180, v106
	v_add_f32_e32 v75, v75, v108
	v_add_f32_e32 v74, v74, v75
	ds_read_b128 v[174:177], v34 offset:38912
	ds_read_b128 v[178:181], v34 offset:39936
	v_add_f32_dpp v74, v74, v74 quad_perm:[1,0,3,2] row_mask:0xf bank_mask:0xf bound_ctrl:1
	s_waitcnt lgkmcnt(7)
	v_mul_f32_e32 v75, v153, v79
	v_add_f32_dpp v74, v74, v74 quad_perm:[2,3,0,1] row_mask:0xf bank_mask:0xf bound_ctrl:1
	v_fmac_f32_e32 v75, v152, v78
	s_waitcnt lgkmcnt(6)
	v_mul_f32_e32 v108, v157, v83
	v_add_f32_dpp v74, v74, v74 row_half_mirror row_mask:0xf bank_mask:0xf bound_ctrl:1
	v_fmac_f32_e32 v108, v156, v82
	s_nop 0
	v_add_f32_dpp v74, v74, v74 row_mirror row_mask:0xf bank_mask:0xf bound_ctrl:1
	s_nop 0
	v_readlane_b32 s14, v74, 0
	v_readlane_b32 s69, v74, 16
	v_readlane_b32 s15, v74, 32
	v_readlane_b32 s70, v74, 48
	v_mul_f32_e32 v74, v151, v77
	v_fmac_f32_e32 v74, v150, v76
	ds_read_b128 v[150:153], v34 offset:40960
	v_add_f32_e32 v74, v74, v75
	v_mul_f32_e32 v75, v155, v85
	v_fmac_f32_e32 v75, v154, v84
	ds_read_b128 v[154:157], v34 offset:41984
	v_add_f32_e32 v74, 0, v74
	v_add_f32_e32 v75, v75, v108
	v_add_f32_e32 v74, v74, v75
	s_waitcnt lgkmcnt(7)
	v_mul_f32_e32 v75, v159, v81
	v_mul_f32_e32 v108, v161, v87
	v_fmac_f32_e32 v75, v158, v80
	v_fmac_f32_e32 v108, v160, v86
	ds_read_b128 v[158:161], v34 offset:43008
	v_add_f32_e32 v75, v75, v108
	v_add_f32_e32 v74, v74, v75
	s_waitcnt lgkmcnt(7)
	v_mul_f32_e32 v75, v163, v91
	v_mul_f32_e32 v108, v165, v89
	v_fmac_f32_e32 v75, v162, v90
	v_fmac_f32_e32 v108, v164, v88
	ds_read_b128 v[162:165], v34 offset:44032
	v_add_f32_e32 v75, v75, v108
	v_add_f32_e32 v74, v74, v75
	s_waitcnt lgkmcnt(7)
	v_mul_f32_e32 v75, v167, v93
	v_mul_f32_e32 v108, v169, v95
	v_fmac_f32_e32 v75, v166, v92
	v_fmac_f32_e32 v108, v168, v94
	ds_read_b128 v[166:169], v34 offset:45056
	v_add_f32_e32 v75, v75, v108
	v_add_f32_e32 v74, v74, v75
	s_waitcnt lgkmcnt(7)
	v_mul_f32_e32 v75, v171, v101
	v_mul_f32_e32 v108, v173, v99
	v_fmac_f32_e32 v75, v170, v100
	v_fmac_f32_e32 v108, v172, v98
	ds_read_b128 v[170:173], v34 offset:46080
	v_add_f32_e32 v75, v75, v108
	v_add_f32_e32 v74, v74, v75
	s_waitcnt lgkmcnt(7)
	v_mul_f32_e32 v75, v175, v97
	v_mul_f32_e32 v108, v177, v103
	v_fmac_f32_e32 v75, v174, v96
	v_fmac_f32_e32 v108, v176, v102
	v_add_f32_e32 v75, v75, v108
	v_add_f32_e32 v74, v74, v75
	s_waitcnt lgkmcnt(6)
	v_mul_f32_e32 v75, v179, v105
	v_mul_f32_e32 v108, v181, v107
	v_fmac_f32_e32 v75, v178, v104
	v_fmac_f32_e32 v108, v180, v106
	v_add_f32_e32 v75, v75, v108
	v_add_f32_e32 v74, v74, v75
	ds_read_b128 v[174:177], v34 offset:47104
	ds_read_b128 v[178:181], v34 offset:48128
	v_add_f32_dpp v74, v74, v74 quad_perm:[1,0,3,2] row_mask:0xf bank_mask:0xf bound_ctrl:1
	s_waitcnt lgkmcnt(7)
	v_mul_f32_e32 v75, v153, v79
	v_add_f32_dpp v74, v74, v74 quad_perm:[2,3,0,1] row_mask:0xf bank_mask:0xf bound_ctrl:1
	v_fmac_f32_e32 v75, v152, v78
	s_waitcnt lgkmcnt(6)
	v_mul_f32_e32 v108, v157, v83
	v_add_f32_dpp v74, v74, v74 row_half_mirror row_mask:0xf bank_mask:0xf bound_ctrl:1
	v_fmac_f32_e32 v108, v156, v82
	s_nop 0
	v_add_f32_dpp v74, v74, v74 row_mirror row_mask:0xf bank_mask:0xf bound_ctrl:1
	s_nop 0
	v_readlane_b32 s16, v74, 0
	v_readlane_b32 s71, v74, 16
	v_readlane_b32 s17, v74, 32
	v_readlane_b32 s72, v74, 48
	v_mul_f32_e32 v74, v151, v77
	v_fmac_f32_e32 v74, v150, v76
	ds_read_b128 v[150:153], v34 offset:49152
	v_add_f32_e32 v74, v74, v75
	v_mul_f32_e32 v75, v155, v85
	v_fmac_f32_e32 v75, v154, v84
	ds_read_b128 v[154:157], v34 offset:50176
	v_add_f32_e32 v74, 0, v74
	v_add_f32_e32 v75, v75, v108
	v_add_f32_e32 v74, v74, v75
	s_waitcnt lgkmcnt(7)
	v_mul_f32_e32 v75, v159, v81
	v_mul_f32_e32 v108, v161, v87
	v_fmac_f32_e32 v75, v158, v80
	v_fmac_f32_e32 v108, v160, v86
	ds_read_b128 v[158:161], v34 offset:51200
	v_add_f32_e32 v75, v75, v108
	v_add_f32_e32 v74, v74, v75
	s_waitcnt lgkmcnt(7)
	v_mul_f32_e32 v75, v163, v91
	v_mul_f32_e32 v108, v165, v89
	v_fmac_f32_e32 v75, v162, v90
	v_fmac_f32_e32 v108, v164, v88
	ds_read_b128 v[162:165], v34 offset:52224
	v_add_f32_e32 v75, v75, v108
	v_add_f32_e32 v74, v74, v75
	s_waitcnt lgkmcnt(7)
	v_mul_f32_e32 v75, v167, v93
	v_mul_f32_e32 v108, v169, v95
	v_fmac_f32_e32 v75, v166, v92
	v_fmac_f32_e32 v108, v168, v94
	ds_read_b128 v[166:169], v34 offset:53248
	v_add_f32_e32 v75, v75, v108
	v_add_f32_e32 v74, v74, v75
	s_waitcnt lgkmcnt(7)
	v_mul_f32_e32 v75, v171, v101
	v_mul_f32_e32 v108, v173, v99
	v_fmac_f32_e32 v75, v170, v100
	v_fmac_f32_e32 v108, v172, v98
	ds_read_b128 v[170:173], v34 offset:54272
	v_add_f32_e32 v75, v75, v108
	v_add_f32_e32 v74, v74, v75
	s_waitcnt lgkmcnt(7)
	v_mul_f32_e32 v75, v175, v97
	v_mul_f32_e32 v108, v177, v103
	v_fmac_f32_e32 v75, v174, v96
	v_fmac_f32_e32 v108, v176, v102
	v_add_f32_e32 v75, v75, v108
	v_add_f32_e32 v74, v74, v75
	s_waitcnt lgkmcnt(6)
	v_mul_f32_e32 v75, v179, v105
	v_mul_f32_e32 v108, v181, v107
	v_fmac_f32_e32 v75, v178, v104
	v_fmac_f32_e32 v108, v180, v106
	v_add_f32_e32 v75, v75, v108
	v_add_f32_e32 v74, v74, v75
	ds_read_b128 v[174:177], v34 offset:55296
	ds_read_b128 v[178:181], v34 offset:56320
	v_add_f32_dpp v74, v74, v74 quad_perm:[1,0,3,2] row_mask:0xf bank_mask:0xf bound_ctrl:1
	s_waitcnt lgkmcnt(7)
	v_mul_f32_e32 v75, v153, v79
	v_add_f32_dpp v74, v74, v74 quad_perm:[2,3,0,1] row_mask:0xf bank_mask:0xf bound_ctrl:1
	v_fmac_f32_e32 v75, v152, v78
	s_waitcnt lgkmcnt(6)
	v_mul_f32_e32 v108, v157, v83
	v_add_f32_dpp v74, v74, v74 row_half_mirror row_mask:0xf bank_mask:0xf bound_ctrl:1
	v_fmac_f32_e32 v108, v156, v82
	s_nop 0
	v_add_f32_dpp v74, v74, v74 row_mirror row_mask:0xf bank_mask:0xf bound_ctrl:1
	s_nop 0
	v_readlane_b32 s18, v74, 0
	v_readlane_b32 s73, v74, 16
	v_readlane_b32 s19, v74, 32
	v_readlane_b32 s74, v74, 48
	v_mul_f32_e32 v74, v151, v77
	v_fmac_f32_e32 v74, v150, v76
	ds_read_b128 v[150:153], v34 offset:57344
	v_add_f32_e32 v74, v74, v75
	v_mul_f32_e32 v75, v155, v85
	v_fmac_f32_e32 v75, v154, v84
	ds_read_b128 v[154:157], v34 offset:58368
	v_add_f32_e32 v74, 0, v74
	v_add_f32_e32 v75, v75, v108
	v_add_f32_e32 v74, v74, v75
	s_waitcnt lgkmcnt(7)
	v_mul_f32_e32 v75, v159, v81
	v_mul_f32_e32 v108, v161, v87
	v_fmac_f32_e32 v75, v158, v80
	v_fmac_f32_e32 v108, v160, v86
	ds_read_b128 v[158:161], v34 offset:59392
	v_add_f32_e32 v75, v75, v108
	v_add_f32_e32 v74, v74, v75
	s_waitcnt lgkmcnt(7)
	v_mul_f32_e32 v75, v163, v91
	v_mul_f32_e32 v108, v165, v89
	v_fmac_f32_e32 v75, v162, v90
	v_fmac_f32_e32 v108, v164, v88
	ds_read_b128 v[162:165], v34 offset:60416
	v_add_f32_e32 v75, v75, v108
	v_add_f32_e32 v74, v74, v75
	s_waitcnt lgkmcnt(7)
	v_mul_f32_e32 v75, v167, v93
	v_mul_f32_e32 v108, v169, v95
	v_fmac_f32_e32 v75, v166, v92
	v_fmac_f32_e32 v108, v168, v94
	ds_read_b128 v[166:169], v34 offset:61440
	v_add_f32_e32 v75, v75, v108
	v_add_f32_e32 v74, v74, v75
	s_waitcnt lgkmcnt(7)
	v_mul_f32_e32 v75, v171, v101
	v_mul_f32_e32 v108, v173, v99
	v_fmac_f32_e32 v75, v170, v100
	v_fmac_f32_e32 v108, v172, v98
	ds_read_b128 v[170:173], v34 offset:62464
	v_add_f32_e32 v75, v75, v108
	v_add_f32_e32 v74, v74, v75
	s_waitcnt lgkmcnt(7)
	v_mul_f32_e32 v75, v175, v97
	v_mul_f32_e32 v108, v177, v103
	v_fmac_f32_e32 v75, v174, v96
	v_fmac_f32_e32 v108, v176, v102
	v_add_f32_e32 v75, v75, v108
	v_add_f32_e32 v74, v74, v75
	s_waitcnt lgkmcnt(6)
	v_mul_f32_e32 v75, v179, v105
	v_mul_f32_e32 v108, v181, v107
	v_fmac_f32_e32 v75, v178, v104
	v_fmac_f32_e32 v108, v180, v106
	v_add_f32_e32 v75, v75, v108
	v_add_f32_e32 v74, v74, v75
	ds_read_b128 v[174:177], v34 offset:63488
	ds_read_b128 v[178:181], v34 offset:64512
	v_add_f32_dpp v74, v74, v74 quad_perm:[1,0,3,2] row_mask:0xf bank_mask:0xf bound_ctrl:1
	s_waitcnt lgkmcnt(7)
	v_mul_f32_e32 v75, v153, v79
	v_add_f32_dpp v74, v74, v74 quad_perm:[2,3,0,1] row_mask:0xf bank_mask:0xf bound_ctrl:1
	v_fmac_f32_e32 v75, v152, v78
	s_waitcnt lgkmcnt(6)
	v_mul_f32_e32 v79, v155, v85
	v_add_f32_dpp v74, v74, v74 row_half_mirror row_mask:0xf bank_mask:0xf bound_ctrl:1
	v_mul_f32_e32 v83, v157, v83
	v_fmac_f32_e32 v79, v154, v84
	v_add_f32_dpp v74, v74, v74 row_mirror row_mask:0xf bank_mask:0xf bound_ctrl:1
	v_fmac_f32_e32 v83, v156, v82
	v_readlane_b32 s20, v74, 0
	v_readlane_b32 s75, v74, 16
	v_readlane_b32 s21, v74, 32
	v_readlane_b32 s76, v74, 48
	v_mul_f32_e32 v74, v151, v77
	v_fmac_f32_e32 v74, v150, v76
	v_add_f32_e32 v74, v74, v75
	v_add_f32_e32 v78, 0, v74
	v_add_f32_e32 v79, v79, v83
	v_add_f32_e32 v78, v78, v79
	s_waitcnt lgkmcnt(5)
	v_mul_f32_e32 v75, v159, v81
	v_fmac_f32_e32 v75, v158, v80
	v_mul_f32_e32 v74, v161, v87
	v_fmac_f32_e32 v74, v160, v86
	v_add_f32_e32 v74, v75, v74
	v_add_f32_e32 v78, v78, v74
	s_waitcnt lgkmcnt(4)
	v_mul_f32_e32 v79, v163, v91
	v_mul_f32_e32 v80, v165, v89
	v_fmac_f32_e32 v79, v162, v90
	v_fmac_f32_e32 v80, v164, v88
	v_add_f32_e32 v79, v79, v80
	v_add_f32_e32 v82, v78, v79
	s_waitcnt lgkmcnt(3)
	v_mul_f32_e32 v75, v167, v93
	v_fmac_f32_e32 v75, v166, v92
	v_mul_f32_e32 v74, v169, v95
	v_fmac_f32_e32 v74, v168, v94
	v_add_f32_e32 v74, v75, v74
	s_waitcnt lgkmcnt(2)
	v_mul_f32_e32 v79, v171, v101
	v_add_f32_e32 v82, v82, v74
	v_fmac_f32_e32 v79, v170, v100
	v_mul_f32_e32 v78, v173, v99
	v_fmac_f32_e32 v78, v172, v98
	v_add_f32_e32 v78, v79, v78
	v_add_f32_e32 v82, v82, v78
	s_waitcnt lgkmcnt(1)
	v_mul_f32_e32 v75, v175, v97
	v_fmac_f32_e32 v75, v174, v96
	v_mul_f32_e32 v74, v177, v103
	v_fmac_f32_e32 v74, v176, v102
	v_add_f32_e32 v74, v75, v74
	s_waitcnt lgkmcnt(0)
	v_mul_f32_e32 v75, v179, v105
	v_mul_f32_e32 v76, v181, v107
	v_fmac_f32_e32 v75, v178, v104
	v_fmac_f32_e32 v76, v180, v106
	v_add_f32_e32 v74, v82, v74
	v_add_f32_e32 v75, v75, v76
	v_add_f32_e32 v74, v74, v75
	s_nop 1
	v_add_f32_dpp v74, v74, v74 quad_perm:[1,0,3,2] row_mask:0xf bank_mask:0xf bound_ctrl:1
	s_nop 1
	v_add_f32_dpp v74, v74, v74 quad_perm:[2,3,0,1] row_mask:0xf bank_mask:0xf bound_ctrl:1
	s_nop 1
	v_add_f32_dpp v74, v74, v74 row_half_mirror row_mask:0xf bank_mask:0xf bound_ctrl:1
	s_nop 1
	v_add_f32_dpp v74, v74, v74 row_mirror row_mask:0xf bank_mask:0xf bound_ctrl:1
	s_nop 0
	v_readlane_b32 s52, v74, 0
	v_readlane_b32 s77, v74, 16
	v_readlane_b32 s53, v74, 32
	v_readlane_b32 s78, v74, 48
	s_and_saveexec_b64 s[48:49], s[4:5]
	s_cbranch_execz .LBB0_1375
	v_readlane_b32 s80, v251, 0
	v_readlane_b32 s82, v251, 2
	v_readlane_b32 s83, v251, 3
	s_nop 4
	v_mov_b32_e32 v74, v234
	v_mov_b32_e32 v75, v235
	v_mov_b32_e32 v76, v236
	v_mov_b32_e32 v77, v237
	v_mov_b32_e32 v78, v238
	v_mov_b32_e32 v79, v239
	v_mov_b32_e32 v80, v240
	v_mov_b32_e32 v81, v241
	v_mov_b32_e32 v82, s77
	v_mov_b32_e32 v83, s78
	v_mov_b32_e32 v94, s64
	v_mov_b32_e32 v95, s65
	v_mov_b32_e32 v96, s39
	v_mov_b32_e32 v97, s63
	v_mov_b32_e32 v84, s75
	v_mov_b32_e32 v85, s76
	v_mov_b32_e32 v86, s73
	v_mov_b32_e32 v87, s74
	v_mov_b32_e32 v88, s71
	v_mov_b32_e32 v89, s72
	v_pk_add_f32 v[82:83], s[52:53], v[82:83]
	v_pk_add_f32 v[94:95], s[6:7], v[94:95]
	v_pk_add_f32 v[96:97], s[0:1], v[96:97]
	v_pk_add_f32 v[84:85], s[20:21], v[84:85]
	v_pk_add_f32 v[86:87], s[18:19], v[86:87]
	v_pk_add_f32 v[88:89], s[16:17], v[88:89]
	v_add_f32_e32 v98, v82, v83
	v_mov_b32_e32 v82, v96
	v_mov_b32_e32 v83, v94
	v_mov_b32_e32 v94, v97
	v_mov_b32_e32 v92, s66
	v_mov_b32_e32 v93, s67
	v_add_f32_e32 v84, v84, v85
	v_add_f32_e32 v85, v86, v87
	v_add_f32_e32 v86, v88, v89
	v_pk_add_f32 v[82:83], v[82:83], v[94:95]
	v_pk_add_f32 v[92:93], s[8:9], v[92:93]
	v_mov_b32_e32 v90, s69
	v_mov_b32_e32 v91, s70
	v_add_f32_e32 v88, v92, v93
	v_pk_add_f32 v[90:91], s[14:15], v[90:91]
	s_mov_b64 s[50:51], exec
	v_add_f32_e32 v87, v90, v91
	v_readlane_b32 s81, v251, 1
	v_readlane_b32 s84, v251, 4
	v_readlane_b32 s85, v251, 5
	v_readlane_b32 s86, v251, 6
	v_readlane_b32 s87, v251, 7
	s_waitcnt vmcnt(0)
	v_add_f32_e32 v76, v76, v84
	v_add_f32_e32 v84, v75, v85
	v_add_f32_e32 v85, v74, v86
	v_pk_add_f32 v[74:75], v[78:79], v[82:83]
	v_add_f32_e32 v80, v80, v88
	v_cmp_gt_f32_e32 vcc, v75, v74
	v_add_f32_e32 v81, v81, v87
	v_add_f32_e32 v77, v77, v98
	v_cndmask_b32_e32 v78, v74, v75, vcc
	v_cmp_gt_f32_e64 s[6:7], v80, v78
	v_cndmask_b32_e64 v79, 0, 1, vcc
	v_cmp_nlt_f32_e64 s[0:1], s62, v74
	v_cndmask_b32_e64 v78, v78, v80, s[6:7]
	v_cmp_gt_f32_e32 vcc, v81, v78
	v_readfirstlane_b32 s39, v79
	s_nop 0
	v_cndmask_b32_e32 v78, v78, v81, vcc
	v_cmp_gt_f32_e64 s[8:9], v85, v78
	s_nop 1
	v_cndmask_b32_e64 v78, v78, v85, s[8:9]
	v_cmp_gt_f32_e64 s[14:15], v84, v78
	s_nop 1
	v_cndmask_b32_e64 v78, v78, v84, s[14:15]
	v_cmp_gt_f32_e64 s[16:17], v76, v78
	s_nop 1
	v_cndmask_b32_e64 v78, v78, v76, s[16:17]
	v_cmp_ngt_f32_e64 s[18:19], v77, v78
	s_and_b64 s[20:21], s[18:19], s[16:17]
	s_and_b64 s[6:7], s[6:7], exec
	s_cselect_b32 s39, 2, s39
	s_and_b64 s[6:7], vcc, exec
	s_cselect_b32 s39, 3, s39
	s_and_b64 s[6:7], s[8:9], exec
	s_cselect_b32 s8, 4, s39
	s_and_b64 s[6:7], s[14:15], exec
	s_cselect_b32 s8, 5, s8
	s_and_b64 s[6:7], s[16:17], exec
	s_cselect_b32 s8, 6, s8
	s_and_b64 s[6:7], s[18:19], exec
	s_cselect_b32 s52, s8, 7
	s_cmp_lg_u32 s52, 5
	s_cselect_b64 s[16:17], -1, 0
	s_cmp_lg_u32 s52, 4
	s_cselect_b64 s[14:15], -1, 0
	s_cmp_lg_u32 s52, 3
	s_cselect_b64 s[8:9], -1, 0
	s_cmp_lg_u32 s52, 2
	s_cselect_b64 s[6:7], -1, 0
	s_cmp_lg_u32 s52, 1
	s_cselect_b64 s[64:65], -1, 0
	s_cmp_eq_u32 s52, 0
	s_cselect_b64 s[66:67], -1, 0
	s_or_b64 vcc, s[66:67], s[0:1]
	v_cndmask_b32_e32 v74, v74, v116, vcc
	v_cmp_gt_f32_e64 s[0:1], v75, v74
	v_cndmask_b32_e64 v79, 0, -1, vcc
	s_and_b64 vcc, s[64:65], s[0:1]
	v_cndmask_b32_e32 v74, v74, v75, vcc
	v_cmp_gt_f32_e64 s[0:1], v80, v74
	s_and_b64 s[0:1], s[6:7], s[0:1]
	v_cndmask_b32_e64 v78, v77, v78, s[18:19]
	v_cndmask_b32_e64 v74, v74, v80, s[0:1]
	v_cmp_gt_f32_e64 s[6:7], v81, v74
	s_and_b64 s[6:7], s[8:9], s[6:7]
	v_readfirstlane_b32 s39, v79
	v_cndmask_b32_e64 v74, v74, v81, s[6:7]
	v_cmp_gt_f32_e64 s[8:9], v85, v74
	s_and_b64 s[8:9], s[14:15], s[8:9]
	s_nop 0
	v_cndmask_b32_e64 v74, v74, v85, s[8:9]
	v_cmp_gt_f32_e64 s[14:15], v84, v74
	s_and_b64 s[14:15], s[16:17], s[14:15]
	s_nop 0
	v_cndmask_b32_e64 v74, v74, v84, s[14:15]
	v_cmp_ngt_f32_e64 s[16:17], v76, v74
	s_or_b64 s[16:17], s[20:21], s[16:17]
	s_nop 0
	v_cndmask_b32_e64 v74, v76, v74, s[16:17]
	v_cmp_gt_f32_e64 s[20:21], v77, v74
	s_and_b64 s[18:19], s[18:19], s[20:21]
	v_cndmask_b32_e64 v74, v74, v77, s[18:19]
	v_sub_f32_e32 v74, v74, v78
	v_mul_f32_e32 v74, 0x3fb8aa3b, v74
	v_exp_f32_e32 v74, v74
	s_and_b64 s[20:21], vcc, exec
	s_cselect_b32 s20, 1, s39
	s_and_b64 s[0:1], s[0:1], exec
	v_add_f32_e32 v74, 1.0, v74
	v_div_scale_f32 v75, s[0:1], v74, v74, 1.0
	v_rcp_f32_e32 v76, v75
	s_cselect_b32 s20, 2, s20
	s_and_b64 s[0:1], s[6:7], exec
	s_cselect_b32 s6, 3, s20
	s_and_b64 s[0:1], s[8:9], exec
	s_cselect_b32 s6, 4, s6
	s_and_b64 s[0:1], s[14:15], exec
	s_cselect_b32 s6, 5, s6
	s_and_b64 s[0:1], s[16:17], exec
	v_fma_f32 v77, -v75, v76, 1.0
	s_cselect_b32 s6, s6, 6
	s_and_b64 s[0:1], s[18:19], exec
	v_fmac_f32_e32 v76, v77, v76
	v_div_scale_f32 v77, vcc, 1.0, v74, 1.0
	s_cselect_b32 s6, 7, s6
	v_mul_f32_e32 v78, v77, v76
	v_fma_f32 v79, -v75, v78, v77
	s_lshl_b32 s0, s6, 8
	v_fmac_f32_e32 v78, v79, v76
	s_add_i32 s7, s0, s52
	v_fma_f32 v75, -v75, v78, v77
	s_add_u32 s0, s56, s28
	v_div_fmas_f32 v75, v75, v76, v78
	s_addc_u32 s1, s57, s29
	v_mov_b32_e32 v76, s7
	s_ashr_i32 s39, s38, 31
	global_store_dword v113, v76, s[0:1] offset:4
	s_lshl_b64 s[0:1], s[38:39], 2
	v_div_fixup_f32 v74, v75, v74, 1.0
	s_add_u32 s0, s30, s0
	v_sub_f32_e32 v75, 1.0, v74
	s_addc_u32 s1, s31, s1
	global_store_dwordx2 v35, v[74:75], s[0:1]
	v_mbcnt_lo_u32_b32 v74, s50, 0
	v_mbcnt_hi_u32_b32 v74, s51, v74
	v_cmp_eq_u32_e32 vcc, 0, v74
	s_and_saveexec_b64 s[0:1], vcc
	s_cbranch_execz .LBB0_1386
	s_lshl_b32 s7, s52, 2
	s_add_i32 s7, s7, 0
	s_add_i32 s7, s7, 0x10000
	s_bcnt1_i32_b64 s8, s[50:51]
	v_mov_b32_e32 v74, s7
	v_mov_b32_e32 v75, s8
	ds_add_u32 v74, v75
